# GDN chunk unit S3: operand LDS reads of product tile t4+1 issued before the epilogue of tile t4 (fresh registers)
# speedup vs baseline: 1.0064x; 1.0064x over previous
; #define LAS __attribute__((address_space(3)))
; __device__ __forceinline__ void gdn_fetch(CArgs& a, int u, int w, int lane, GdnIn& in) {
;     const int chain = u / 36, n = u % 36, b = chain >> 3, h = (chain >> 1) & 3, dir = chain & 1;
;     const int r0 = scan_row(b, dir, n * 64), step = dir ? -1 : 1, fr = lane & 15, kg = lane >> 4;
;     const float* DQ = (const float*)(a.ws + WS_MIX + MX_DQ) + h * 64; const float* DK = (const float*)(a.ws + WS_MIX + MX_DK) + h * 64; const float* DV = (const float*)(a.ws + WS_MIX + MX_DV) + h * 64;
;     const float* DG = (const float*)(a.ws + WS_MIX + MX_DG);
;     const bf16* KB = (const bf16*)(a.ws + WS_CKD + CD_KB) + (ptrdiff_t)r0 * 256 + h * 64; const bf16* QB = (const bf16*)(a.ws + WS_CKD + CD_QB) + (ptrdiff_t)r0 * 256 + h * 64;
;     const ptrdiff_t ldt = (ptrdiff_t)step * 256;
;     const bool isW = w >= 4; const int c0 = 16 * (w & 3), I1 = w >> 1;
;     in.g2 = *(const f32x2*)(DG + (size_t)(r0 + step * lane) * 16 + h * 4 + dir * 2);
; #pragma unroll
;     for (int s = 0; s < 2; ++s) { in.ak[s] = *(const bf16x8*)(KB + (ptrdiff_t)(16 * I1 + fr) * ldt + 32 * s + 8 * kg); in.aq[s] = *(const bf16x8*)(QB + (ptrdiff_t)(16 * I1 + fr) * ldt + 32 * s + 8 * kg);
; #pragma unroll
;         for (int jj = 0; jj < 2; ++jj) in.bk[jj][s] = *(const bf16x8*)(KB + (ptrdiff_t)(16 * (2 * (w & 1) + jj) + fr) * ldt + 32 * s + 8 * kg); }
; #pragma unroll
;     for (int tt = 0; tt < 8; ++tt) in.kt8[tt] = KB[(ptrdiff_t)(8 * w + tt) * ldt + lane];
; __device__ __forceinline__ void gdn_s23(CArgs& a, int u, const GdnIn2& in, LAS unsigned char* ub, LAS unsigned char* dwb, int w, int lane, float cl) {
;     ...
;     { const int blk = lane >> 4, c = lane & 15; float T[16];
; #pragma unroll
;       for (int hb = 0; hb < 4; ++hb) {
;           u32x4 arow[4][2];
; #pragma unroll
;           for (int rr = 0; rr < 4; ++rr) { const int r = 4 * hb + rr; arow[rr][0] = *(const LAS u32x4*)(AB + (16 * blk + r) * 72 + 16 * blk); if (hb >= 2) arow[rr][1] = *(const LAS u32x4*)(AB + (16 * blk + r) * 72 + 16 * blk + 8); }
;           asm volatile("s_waitcnt lgkmcnt(0)" ::: "memory");
; #pragma unroll
;           for (int rr = 0; rr < 4; ++rr) { const int r = 4 * hb + rr; float t = (r == c) ? 1.f : 0.f;
;               float t2 = 0.f;
; #pragma unroll
.LBB0_1723:
	s_bfe_u32 s76, s9, 0x20001
	s_cmp_eq_u32 s27, 0
	s_cselect_b64 s[52:53], -1, 0
	s_and_b64 s[48:49], s[52:53], exec
	s_cselect_b32 s77, 1, -1
	s_ashr_i32 s3, s2, 31
	s_lshl_b64 s[48:49], s[2:3], 9
	v_readlane_b32 s3, v251, 14
	s_add_u32 s3, s3, s48
	v_readlane_b32 s54, v249, 10
	s_addc_u32 s55, s54, s49
	s_lshl_b32 s62, s76, 7
	s_add_u32 s54, s3, s62
	s_addc_u32 s55, s55, 0
	s_add_u32 s3, s37, s48
	s_addc_u32 s49, s72, s49
	v_mul_lo_u32 v46, v110, s77
	s_add_u32 s48, s3, s62
	v_add_u32_e32 v46, s2, v46
	s_addc_u32 s49, s49, 0
	v_ashrrev_i32_e32 v47, 31, v46
	s_and_b64 s[62:63], s[52:53], exec
	s_movk_i32 s3, 0xff00
	v_lshlrev_b64 v[46:47], 6, v[46:47]
	s_cselect_b32 s62, 0x100, s3
	v_lshl_add_u64 v[46:47], s[6:7], 0, v[46:47]
	s_lshl_b32 s78, s76, 4
	v_lshl_add_u64 v[46:47], v[46:47], 0, s[78:79]
	s_lshl_b32 s78, s27, 3
	v_lshl_add_u64 v[46:47], v[46:47], 0, s[78:79]
	global_load_dwordx2 v[114:115], v[46:47], off
	v_or_b32_e32 v46, s42, v119
	v_ashrrev_i32_e32 v50, 1, v110
	v_mad_i64_i32 v[46:47], s[2:3], s62, v46, 0
	v_and_b32_e32 v50, -8, v50
	v_lshlrev_b64 v[46:47], 1, v[46:47]
	v_ashrrev_i32_e32 v51, 31, v50
	v_lshl_add_u64 v[48:49], s[54:55], 0, v[46:47]
	v_lshlrev_b64 v[50:51], 1, v[50:51]
	v_lshl_add_u64 v[46:47], s[48:49], 0, v[46:47]
	v_lshl_add_u64 v[52:53], v[48:49], 0, v[50:51]
	v_lshl_add_u64 v[54:55], v[46:47], 0, v[50:51]
	v_lshl_add_u64 v[50:51], s[54:55], 0, v[50:51]
	v_mul_hi_i32_i24_e32 v57, s62, v32
	v_mul_i32_i24_e32 v56, s62, v32
	v_lshl_add_u64 v[66:67], v[56:57], 1, v[50:51]
	v_mul_hi_i32_i24_e32 v57, s62, v33
	v_mul_i32_i24_e32 v56, s62, v33
	v_lshl_add_u64 v[32:33], v[56:57], 1, v[50:51]
	v_ashrrev_i32_e32 v111, 31, v110
	global_load_dwordx4 v[58:61], v[52:53], off
	global_load_dwordx4 v[46:49], v[54:55], off
	global_load_dwordx4 v[70:73], v[66:67], off
	global_load_dwordx4 v[62:65], v[32:33], off
	s_nop 0
	global_load_dwordx4 v[50:53], v[52:53], off offset:64
	s_nop 0
	global_load_dwordx4 v[54:57], v[54:55], off offset:64
	s_nop 0
	global_load_dwordx4 v[74:77], v[66:67], off offset:64
	s_nop 0
	global_load_dwordx4 v[66:69], v[32:33], off offset:64
	v_lshl_add_u64 v[32:33], v[110:111], 1, s[54:55]
	s_mul_hi_i32 s3, s62, s73
	s_mul_i32 s2, s62, s73
	v_lshl_add_u64 v[86:87], s[2:3], 1, v[32:33]
	s_mul_hi_i32 s3, s62, s16
	s_mul_i32 s2, s62, s16
	global_load_ushort v131, v[86:87], off
	v_lshl_add_u64 v[86:87], s[2:3], 1, v[32:33]
	s_mul_hi_i32 s3, s62, s17
	s_mul_i32 s2, s62, s17
	global_load_ushort v133, v[86:87], off
	v_lshl_add_u64 v[86:87], s[2:3], 1, v[32:33]
	s_mul_hi_i32 s3, s62, s35
	s_mul_i32 s2, s62, s35
	global_load_ushort v135, v[86:87], off
	v_lshl_add_u64 v[86:87], s[2:3], 1, v[32:33]
	s_mul_hi_i32 s3, s62, s14
	s_mul_i32 s2, s62, s14
	global_load_ushort v137, v[86:87], off
	v_lshl_add_u64 v[86:87], s[2:3], 1, v[32:33]
	s_mul_hi_i32 s3, s62, s82
	s_mul_i32 s2, s62, s82
	global_load_ushort v111, v[86:87], off
	v_lshl_add_u64 v[86:87], s[2:3], 1, v[32:33]
	s_mul_hi_i32 s3, s62, s83
	s_mul_i32 s2, s62, s83
	global_load_ushort v132, v[86:87], off
	v_lshl_add_u64 v[86:87], s[2:3], 1, v[32:33]
	s_mul_hi_i32 s3, s62, s10
	s_mul_i32 s2, s62, s10
	v_lshl_add_u64 v[32:33], s[2:3], 1, v[32:33]
	v_and_b32_e32 v85, -16, v110
	global_load_ushort v134, v[86:87], off
	global_load_ushort v136, v[32:33], off
	v_lshlrev_b32_e32 v118, 1, v119
	v_mov_b32_e32 v225, 1.0
	v_mul_u32_u24_e32 v222, 0x92, v85
	v_lshlrev_b32_e32 v224, 5, v110
	v_and_b32_e32 v224, 0xfffffe00, v224
	v_add3_u32 v223, s8, v118, v224
	v_cmp_eq_u32_e32 vcc, 0, v119
	ds_read_b128 v[86:89], v222 offset:144
	ds_read_b128 v[98:101], v222 offset:288
	ds_read_b128 v[106:109], v222 offset:432
	ds_read_b128 v[170:173], v222 offset:576
	v_cndmask_b32_e32 v202, 0, v225, vcc
	ds_write_b16_d16_hi v223, v202 offset:55296
	ds_read_b128 v[226:229], v222 offset:720
	ds_read_b128 v[234:237], v222 offset:864
	s_waitcnt lgkmcnt(5)
	v_cmp_eq_u32_e32 vcc, 1, v119
	s_nop 1
	v_cndmask_b32_e32 v218, 0, v225, vcc
	v_lshlrev_b32_e32 v220, 16, v86
	v_fma_f32 v203, -v220, v202, v218
	v_cvt_pk_bf16_f32 v224, v203, v203
	ds_write_b16 v223, v224 offset:55328
	v_cmp_eq_u32_e32 vcc, 2, v119
	v_mov_b32_e32 v219, 0
	v_lshlrev_b32_e32 v220, 16, v98
	v_and_b32_e32 v221, 0xffff0000, v98
	v_cndmask_b32_e32 v218, 0, v225, vcc
	v_pk_fma_f32 v[218:219], v[220:221], v[202:203], v[218:219] neg_lo:[1,0,0] neg_hi:[1,0,0]
	v_add_f32_e32 v204, v218, v219
	v_cvt_pk_bf16_f32 v224, v204, v204
	ds_write_b16 v223, v224 offset:55360
	ds_read_b128 v[86:89], v222 offset:1008
	ds_read_b128 v[98:101], v222 offset:1152
	s_waitcnt lgkmcnt(7)
	v_cmp_eq_u32_e32 vcc, 3, v119
	v_mov_b32_e32 v219, 0
	v_lshlrev_b32_e32 v220, 16, v106
	v_and_b32_e32 v221, 0xffff0000, v106
	v_cndmask_b32_e32 v218, 0, v225, vcc
	v_pk_fma_f32 v[218:219], v[220:221], v[202:203], v[218:219] neg_lo:[1,0,0] neg_hi:[1,0,0]
	v_lshlrev_b32_e32 v220, 16, v107
	v_fma_f32 v218, -v220, v204, v218
	v_add_f32_e32 v205, v218, v219
	v_cvt_pk_bf16_f32 v224, v205, v205
	ds_write_b16 v223, v224 offset:55392
	v_cmp_eq_u32_e32 vcc, 4, v119
	v_mov_b32_e32 v219, 0
	v_lshlrev_b32_e32 v220, 16, v170
	v_and_b32_e32 v221, 0xffff0000, v170
	v_cndmask_b32_e32 v218, 0, v225, vcc
	v_pk_fma_f32 v[218:219], v[220:221], v[202:203], v[218:219] neg_lo:[1,0,0] neg_hi:[1,0,0]
	v_lshlrev_b32_e32 v220, 16, v171
	v_and_b32_e32 v221, 0xffff0000, v171
	v_pk_fma_f32 v[218:219], v[220:221], v[204:205], v[218:219] neg_lo:[1,0,0] neg_hi:[1,0,0]
	v_add_f32_e32 v206, v218, v219
	v_cvt_pk_bf16_f32 v224, v206, v206
	ds_write_b16 v223, v224 offset:55424
	ds_read_b128 v[106:109], v222 offset:1296
	ds_read_b128 v[154:157], v222 offset:1312
	ds_read_b128 v[170:173], v222 offset:1440
	ds_read_b128 v[174:177], v222 offset:1456
	s_waitcnt lgkmcnt(10)
; #define LAS __attribute__((address_space(3)))
; __device__ __forceinline__ unsigned f2bf(float f) { unsigned u = __float_as_uint(f); return (u + 0x7fffu + ((u >> 16) & 1u)) >> 16; }
; __device__ __forceinline__ float lo_bf(unsigned w) { return __uint_as_float(w << 16); }
; __device__ __forceinline__ float hi_bf(unsigned w) { return __uint_as_float(w & 0xffff0000u); }
; __device__ __forceinline__ void gdn_s23(CArgs& a, int u, const GdnIn2& in, LAS unsigned char* ub, LAS unsigned char* dwb, int w, int lane, float cl) {
;     ...
;     { const int blk = lane >> 4, c = lane & 15; float T[16];
; #pragma unroll
;       for (int hb = 0; hb < 4; ++hb) {
;           u32x4 arow[4][2];
; #pragma unroll
;           for (int rr = 0; rr < 4; ++rr) { const int r = 4 * hb + rr; arow[rr][0] = *(const LAS u32x4*)(AB + (16 * blk + r) * 72 + 16 * blk); if (hb >= 2) arow[rr][1] = *(const LAS u32x4*)(AB + (16 * blk + r) * 72 + 16 * blk + 8); }
;           asm volatile("s_waitcnt lgkmcnt(0)" ::: "memory");
; #pragma unroll
;           for (int rr = 0; rr < 4; ++rr) { const int r = 4 * hb + rr; float t = (r == c) ? 1.f : 0.f;
;               float t2 = 0.f;
; #pragma unroll
;               for (int j = 0; j < r; ++j) { const unsigned wv = arow[rr][j >> 3][(j >> 1) & 3]; const float av = (j & 1) ? hi_bf(wv) : lo_bf(wv); if (j & 1) t2 -= av * T[j]; else t -= av * T[j]; }
;               t += t2;
;               T[r] = t; DW[(blk * 16 + r) * 16 + c] = (bf16)f2bf(t); } } }
	v_cmp_eq_u32_e32 vcc, 5, v119
	v_mov_b32_e32 v219, 0
	v_lshlrev_b32_e32 v220, 16, v226
	v_and_b32_e32 v221, 0xffff0000, v226
	v_cndmask_b32_e32 v218, 0, v225, vcc
	v_pk_fma_f32 v[218:219], v[220:221], v[202:203], v[218:219] neg_lo:[1,0,0] neg_hi:[1,0,0]
	v_lshlrev_b32_e32 v220, 16, v227
	v_and_b32_e32 v221, 0xffff0000, v227
	v_pk_fma_f32 v[218:219], v[220:221], v[204:205], v[218:219] neg_lo:[1,0,0] neg_hi:[1,0,0]
	v_lshlrev_b32_e32 v220, 16, v228
	v_fma_f32 v218, -v220, v206, v218
	v_add_f32_e32 v207, v218, v219
	v_cvt_pk_bf16_f32 v224, v207, v207
	ds_write_b16 v223, v224 offset:55456
	v_cmp_eq_u32_e32 vcc, 6, v119
	v_mov_b32_e32 v219, 0
	v_lshlrev_b32_e32 v220, 16, v234
	v_and_b32_e32 v221, 0xffff0000, v234
	v_cndmask_b32_e32 v218, 0, v225, vcc
	v_pk_fma_f32 v[218:219], v[220:221], v[202:203], v[218:219] neg_lo:[1,0,0] neg_hi:[1,0,0]
	v_lshlrev_b32_e32 v220, 16, v235
	v_and_b32_e32 v221, 0xffff0000, v235
	v_pk_fma_f32 v[218:219], v[220:221], v[204:205], v[218:219] neg_lo:[1,0,0] neg_hi:[1,0,0]
	v_lshlrev_b32_e32 v220, 16, v236
	v_and_b32_e32 v221, 0xffff0000, v236
	v_pk_fma_f32 v[218:219], v[220:221], v[206:207], v[218:219] neg_lo:[1,0,0] neg_hi:[1,0,0]
	v_add_f32_e32 v208, v218, v219
	v_cvt_pk_bf16_f32 v224, v208, v208
	ds_write_b16 v223, v224 offset:55488
	ds_read_b128 v[226:229], v222 offset:1584
	ds_read_b128 v[230:233], v222 offset:1600
	ds_read_b128 v[234:237], v222 offset:1728
	ds_read_b128 v[238:241], v222 offset:1744
	s_waitcnt lgkmcnt(12)
	v_cmp_eq_u32_e32 vcc, 7, v119
	v_mov_b32_e32 v219, 0
	v_lshlrev_b32_e32 v220, 16, v86
	v_and_b32_e32 v221, 0xffff0000, v86
	v_cndmask_b32_e32 v218, 0, v225, vcc
	v_pk_fma_f32 v[218:219], v[220:221], v[202:203], v[218:219] neg_lo:[1,0,0] neg_hi:[1,0,0]
	v_lshlrev_b32_e32 v220, 16, v87
	v_and_b32_e32 v221, 0xffff0000, v87
	v_pk_fma_f32 v[218:219], v[220:221], v[204:205], v[218:219] neg_lo:[1,0,0] neg_hi:[1,0,0]
	v_lshlrev_b32_e32 v220, 16, v88
	v_and_b32_e32 v221, 0xffff0000, v88
	v_pk_fma_f32 v[218:219], v[220:221], v[206:207], v[218:219] neg_lo:[1,0,0] neg_hi:[1,0,0]
	v_lshlrev_b32_e32 v220, 16, v89
	v_fma_f32 v218, -v220, v208, v218
	v_add_f32_e32 v209, v218, v219
	v_cvt_pk_bf16_f32 v224, v209, v209
	ds_write_b16 v223, v224 offset:55520
	v_cmp_eq_u32_e32 vcc, 8, v119
	v_mov_b32_e32 v219, 0
	v_lshlrev_b32_e32 v220, 16, v98
	v_and_b32_e32 v221, 0xffff0000, v98
	v_cndmask_b32_e32 v218, 0, v225, vcc
	v_pk_fma_f32 v[218:219], v[220:221], v[202:203], v[218:219] neg_lo:[1,0,0] neg_hi:[1,0,0]
	v_lshlrev_b32_e32 v220, 16, v99
	v_and_b32_e32 v221, 0xffff0000, v99
	v_pk_fma_f32 v[218:219], v[220:221], v[204:205], v[218:219] neg_lo:[1,0,0] neg_hi:[1,0,0]
	v_lshlrev_b32_e32 v220, 16, v100
	v_and_b32_e32 v221, 0xffff0000, v100
	v_pk_fma_f32 v[218:219], v[220:221], v[206:207], v[218:219] neg_lo:[1,0,0] neg_hi:[1,0,0]
	v_lshlrev_b32_e32 v220, 16, v101
	v_and_b32_e32 v221, 0xffff0000, v101
	v_pk_fma_f32 v[218:219], v[220:221], v[208:209], v[218:219] neg_lo:[1,0,0] neg_hi:[1,0,0]
	v_add_f32_e32 v210, v218, v219
	v_cvt_pk_bf16_f32 v224, v210, v210
	ds_write_b16 v223, v224 offset:55552
	ds_read_b128 v[86:89], v222 offset:1872
	ds_read_b128 v[94:97], v222 offset:1888
	ds_read_b128 v[98:101], v222 offset:2016
	ds_read_b128 v[102:105], v222 offset:2032
	s_waitcnt lgkmcnt(12)
	v_cmp_eq_u32_e32 vcc, 9, v119
	v_mov_b32_e32 v219, 0
	v_lshlrev_b32_e32 v220, 16, v106
	v_and_b32_e32 v221, 0xffff0000, v106
	v_cndmask_b32_e32 v218, 0, v225, vcc
	v_pk_fma_f32 v[218:219], v[220:221], v[202:203], v[218:219] neg_lo:[1,0,0] neg_hi:[1,0,0]
	v_lshlrev_b32_e32 v220, 16, v107
	v_and_b32_e32 v221, 0xffff0000, v107
	v_pk_fma_f32 v[218:219], v[220:221], v[204:205], v[218:219] neg_lo:[1,0,0] neg_hi:[1,0,0]
	v_lshlrev_b32_e32 v220, 16, v108
	v_and_b32_e32 v221, 0xffff0000, v108
	v_pk_fma_f32 v[218:219], v[220:221], v[206:207], v[218:219] neg_lo:[1,0,0] neg_hi:[1,0,0]
	v_lshlrev_b32_e32 v220, 16, v109
	v_and_b32_e32 v221, 0xffff0000, v109
	v_pk_fma_f32 v[218:219], v[220:221], v[208:209], v[218:219] neg_lo:[1,0,0] neg_hi:[1,0,0]
	v_lshlrev_b32_e32 v220, 16, v154
	v_fma_f32 v218, -v220, v210, v218
	v_add_f32_e32 v211, v218, v219
	v_cvt_pk_bf16_f32 v224, v211, v211
	ds_write_b16 v223, v224 offset:55584
	v_cmp_eq_u32_e32 vcc, 10, v119
	v_mov_b32_e32 v219, 0
	v_lshlrev_b32_e32 v220, 16, v170
	v_and_b32_e32 v221, 0xffff0000, v170
	v_cndmask_b32_e32 v218, 0, v225, vcc
	v_pk_fma_f32 v[218:219], v[220:221], v[202:203], v[218:219] neg_lo:[1,0,0] neg_hi:[1,0,0]
	v_lshlrev_b32_e32 v220, 16, v171
	v_and_b32_e32 v221, 0xffff0000, v171
	v_pk_fma_f32 v[218:219], v[220:221], v[204:205], v[218:219] neg_lo:[1,0,0] neg_hi:[1,0,0]
	v_lshlrev_b32_e32 v220, 16, v172
	v_and_b32_e32 v221, 0xffff0000, v172
	v_pk_fma_f32 v[218:219], v[220:221], v[206:207], v[218:219] neg_lo:[1,0,0] neg_hi:[1,0,0]
	v_lshlrev_b32_e32 v220, 16, v173
	v_and_b32_e32 v221, 0xffff0000, v173
	v_pk_fma_f32 v[218:219], v[220:221], v[208:209], v[218:219] neg_lo:[1,0,0] neg_hi:[1,0,0]
	v_lshlrev_b32_e32 v220, 16, v174
	v_and_b32_e32 v221, 0xffff0000, v174
	v_pk_fma_f32 v[218:219], v[220:221], v[210:211], v[218:219] neg_lo:[1,0,0] neg_hi:[1,0,0]
	v_add_f32_e32 v212, v218, v219
	v_cvt_pk_bf16_f32 v224, v212, v212
	ds_write_b16 v223, v224 offset:55616
	ds_read_b128 v[106:109], v222 offset:2160
	ds_read_b128 v[154:157], v222 offset:2176
	s_waitcnt lgkmcnt(10)
; #define LAS __attribute__((address_space(3)))
; __device__ __forceinline__ unsigned f2bf(float f) { unsigned u = __float_as_uint(f); return (u + 0x7fffu + ((u >> 16) & 1u)) >> 16; }
; __device__ __forceinline__ float lo_bf(unsigned w) { return __uint_as_float(w << 16); }
; __device__ __forceinline__ float hi_bf(unsigned w) { return __uint_as_float(w & 0xffff0000u); }
; __device__ __forceinline__ void gdn_s23(CArgs& a, int u, const GdnIn2& in, LAS unsigned char* ub, LAS unsigned char* dwb, int w, int lane, float cl) {
;     ...
;     { const int blk = lane >> 4, c = lane & 15; float T[16];
; #pragma unroll
;       for (int hb = 0; hb < 4; ++hb) {
;           u32x4 arow[4][2];
; #pragma unroll
;           for (int rr = 0; rr < 4; ++rr) { const int r = 4 * hb + rr; arow[rr][0] = *(const LAS u32x4*)(AB + (16 * blk + r) * 72 + 16 * blk); if (hb >= 2) arow[rr][1] = *(const LAS u32x4*)(AB + (16 * blk + r) * 72 + 16 * blk + 8); }
;           asm volatile("s_waitcnt lgkmcnt(0)" ::: "memory");
; #pragma unroll
;           for (int rr = 0; rr < 4; ++rr) { const int r = 4 * hb + rr; float t = (r == c) ? 1.f : 0.f;
;               float t2 = 0.f;
; #pragma unroll
;               for (int j = 0; j < r; ++j) { const unsigned wv = arow[rr][j >> 3][(j >> 1) & 3]; const float av = (j & 1) ? hi_bf(wv) : lo_bf(wv); if (j & 1) t2 -= av * T[j]; else t -= av * T[j]; }
;               t += t2;
;               T[r] = t; DW[(blk * 16 + r) * 16 + c] = (bf16)f2bf(t); } } }
;     asm volatile("s_waitcnt lgkmcnt(0)" ::: "memory");
;     f32x4 X[4];
; #pragma unroll
;     for (int I = 0; I < 4; ++I) {
;         const f32x4 br = *(const LAS f32x4*)(GT + 16 * I + 4 * kg), er = *(const LAS f32x4*)(GT + 128 + 16 * I + 4 * kg);
;         const f32x4 Rf = (f32x4){__uint_as_float(in.R[I].x << 16), __uint_as_float(in.R[I].y << 16), __uint_as_float(in.R[I].z << 16), __uint_as_float(in.R[I].w << 16)};
	v_cmp_eq_u32_e32 vcc, 11, v119
	v_mov_b32_e32 v219, 0
	v_lshlrev_b32_e32 v220, 16, v226
	v_and_b32_e32 v221, 0xffff0000, v226
	v_cndmask_b32_e32 v218, 0, v225, vcc
	v_pk_fma_f32 v[218:219], v[220:221], v[202:203], v[218:219] neg_lo:[1,0,0] neg_hi:[1,0,0]
	v_lshlrev_b32_e32 v220, 16, v227
	v_and_b32_e32 v221, 0xffff0000, v227
	v_pk_fma_f32 v[218:219], v[220:221], v[204:205], v[218:219] neg_lo:[1,0,0] neg_hi:[1,0,0]
	v_lshlrev_b32_e32 v220, 16, v228
	v_and_b32_e32 v221, 0xffff0000, v228
	v_pk_fma_f32 v[218:219], v[220:221], v[206:207], v[218:219] neg_lo:[1,0,0] neg_hi:[1,0,0]
	v_lshlrev_b32_e32 v220, 16, v229
	v_and_b32_e32 v221, 0xffff0000, v229
	v_pk_fma_f32 v[218:219], v[220:221], v[208:209], v[218:219] neg_lo:[1,0,0] neg_hi:[1,0,0]
	v_lshlrev_b32_e32 v220, 16, v230
	v_and_b32_e32 v221, 0xffff0000, v230
	v_pk_fma_f32 v[218:219], v[220:221], v[210:211], v[218:219] neg_lo:[1,0,0] neg_hi:[1,0,0]
	v_lshlrev_b32_e32 v220, 16, v231
	v_fma_f32 v218, -v220, v212, v218
	v_add_f32_e32 v213, v218, v219
	v_cvt_pk_bf16_f32 v224, v213, v213
	ds_write_b16 v223, v224 offset:55648
	v_cmp_eq_u32_e32 vcc, 12, v119
	v_mov_b32_e32 v219, 0
	v_lshlrev_b32_e32 v220, 16, v234
	v_and_b32_e32 v221, 0xffff0000, v234
	v_cndmask_b32_e32 v218, 0, v225, vcc
	v_pk_fma_f32 v[218:219], v[220:221], v[202:203], v[218:219] neg_lo:[1,0,0] neg_hi:[1,0,0]
	v_lshlrev_b32_e32 v220, 16, v235
	v_and_b32_e32 v221, 0xffff0000, v235
	v_pk_fma_f32 v[218:219], v[220:221], v[204:205], v[218:219] neg_lo:[1,0,0] neg_hi:[1,0,0]
	v_lshlrev_b32_e32 v220, 16, v236
	v_and_b32_e32 v221, 0xffff0000, v236
	v_pk_fma_f32 v[218:219], v[220:221], v[206:207], v[218:219] neg_lo:[1,0,0] neg_hi:[1,0,0]
	v_lshlrev_b32_e32 v220, 16, v237
	v_and_b32_e32 v221, 0xffff0000, v237
	v_pk_fma_f32 v[218:219], v[220:221], v[208:209], v[218:219] neg_lo:[1,0,0] neg_hi:[1,0,0]
	v_lshlrev_b32_e32 v220, 16, v238
	v_and_b32_e32 v221, 0xffff0000, v238
	v_pk_fma_f32 v[218:219], v[220:221], v[210:211], v[218:219] neg_lo:[1,0,0] neg_hi:[1,0,0]
	v_lshlrev_b32_e32 v220, 16, v239
	v_and_b32_e32 v221, 0xffff0000, v239
	v_pk_fma_f32 v[218:219], v[220:221], v[212:213], v[218:219] neg_lo:[1,0,0] neg_hi:[1,0,0]
	v_add_f32_e32 v214, v218, v219
	v_cvt_pk_bf16_f32 v224, v214, v214
	ds_write_b16 v223, v224 offset:55680
	s_waitcnt lgkmcnt(6)
	v_cmp_eq_u32_e32 vcc, 13, v119
	v_mov_b32_e32 v219, 0
	v_lshlrev_b32_e32 v220, 16, v86
	v_and_b32_e32 v221, 0xffff0000, v86
	v_cndmask_b32_e32 v218, 0, v225, vcc
	v_pk_fma_f32 v[218:219], v[220:221], v[202:203], v[218:219] neg_lo:[1,0,0] neg_hi:[1,0,0]
	v_lshlrev_b32_e32 v220, 16, v87
	v_and_b32_e32 v221, 0xffff0000, v87
	v_pk_fma_f32 v[218:219], v[220:221], v[204:205], v[218:219] neg_lo:[1,0,0] neg_hi:[1,0,0]
	v_lshlrev_b32_e32 v220, 16, v88
	v_and_b32_e32 v221, 0xffff0000, v88
	v_pk_fma_f32 v[218:219], v[220:221], v[206:207], v[218:219] neg_lo:[1,0,0] neg_hi:[1,0,0]
	v_lshlrev_b32_e32 v220, 16, v89
	v_and_b32_e32 v221, 0xffff0000, v89
	v_pk_fma_f32 v[218:219], v[220:221], v[208:209], v[218:219] neg_lo:[1,0,0] neg_hi:[1,0,0]
	v_lshlrev_b32_e32 v220, 16, v94
	v_and_b32_e32 v221, 0xffff0000, v94
	v_pk_fma_f32 v[218:219], v[220:221], v[210:211], v[218:219] neg_lo:[1,0,0] neg_hi:[1,0,0]
	v_lshlrev_b32_e32 v220, 16, v95
	v_and_b32_e32 v221, 0xffff0000, v95
	v_pk_fma_f32 v[218:219], v[220:221], v[212:213], v[218:219] neg_lo:[1,0,0] neg_hi:[1,0,0]
	v_lshlrev_b32_e32 v220, 16, v96
	v_fma_f32 v218, -v220, v214, v218
	v_add_f32_e32 v215, v218, v219
	v_cvt_pk_bf16_f32 v224, v215, v215
	ds_write_b16 v223, v224 offset:55712
	v_cmp_eq_u32_e32 vcc, 14, v119
	v_mov_b32_e32 v219, 0
	v_lshlrev_b32_e32 v220, 16, v98
	v_and_b32_e32 v221, 0xffff0000, v98
	v_cndmask_b32_e32 v218, 0, v225, vcc
	v_pk_fma_f32 v[218:219], v[220:221], v[202:203], v[218:219] neg_lo:[1,0,0] neg_hi:[1,0,0]
	v_lshlrev_b32_e32 v220, 16, v99
	v_and_b32_e32 v221, 0xffff0000, v99
	v_pk_fma_f32 v[218:219], v[220:221], v[204:205], v[218:219] neg_lo:[1,0,0] neg_hi:[1,0,0]
	v_lshlrev_b32_e32 v220, 16, v100
	v_and_b32_e32 v221, 0xffff0000, v100
	v_pk_fma_f32 v[218:219], v[220:221], v[206:207], v[218:219] neg_lo:[1,0,0] neg_hi:[1,0,0]
	v_lshlrev_b32_e32 v220, 16, v101
	v_and_b32_e32 v221, 0xffff0000, v101
	v_pk_fma_f32 v[218:219], v[220:221], v[208:209], v[218:219] neg_lo:[1,0,0] neg_hi:[1,0,0]
	v_lshlrev_b32_e32 v220, 16, v102
	v_and_b32_e32 v221, 0xffff0000, v102
	v_pk_fma_f32 v[218:219], v[220:221], v[210:211], v[218:219] neg_lo:[1,0,0] neg_hi:[1,0,0]
	v_lshlrev_b32_e32 v220, 16, v103
	v_and_b32_e32 v221, 0xffff0000, v103
	v_pk_fma_f32 v[218:219], v[220:221], v[212:213], v[218:219] neg_lo:[1,0,0] neg_hi:[1,0,0]
	v_lshlrev_b32_e32 v220, 16, v104
	v_and_b32_e32 v221, 0xffff0000, v104
	v_pk_fma_f32 v[218:219], v[220:221], v[214:215], v[218:219] neg_lo:[1,0,0] neg_hi:[1,0,0]
	v_add_f32_e32 v216, v218, v219
	v_cvt_pk_bf16_f32 v224, v216, v216
	ds_write_b16 v223, v224 offset:55744
	s_waitcnt lgkmcnt(4)
	v_cmp_eq_u32_e32 vcc, 15, v119
	v_mov_b32_e32 v219, 0
	v_lshlrev_b32_e32 v220, 16, v106
	v_and_b32_e32 v221, 0xffff0000, v106
	v_cndmask_b32_e32 v218, 0, v225, vcc
	v_pk_fma_f32 v[218:219], v[220:221], v[202:203], v[218:219] neg_lo:[1,0,0] neg_hi:[1,0,0]
	v_lshlrev_b32_e32 v220, 16, v107
	v_and_b32_e32 v221, 0xffff0000, v107
	v_pk_fma_f32 v[218:219], v[220:221], v[204:205], v[218:219] neg_lo:[1,0,0] neg_hi:[1,0,0]
	v_lshlrev_b32_e32 v220, 16, v108
	v_and_b32_e32 v221, 0xffff0000, v108
	v_pk_fma_f32 v[218:219], v[220:221], v[206:207], v[218:219] neg_lo:[1,0,0] neg_hi:[1,0,0]
	v_lshlrev_b32_e32 v220, 16, v109
	v_and_b32_e32 v221, 0xffff0000, v109
	v_pk_fma_f32 v[218:219], v[220:221], v[208:209], v[218:219] neg_lo:[1,0,0] neg_hi:[1,0,0]
	v_lshlrev_b32_e32 v220, 16, v154
	v_and_b32_e32 v221, 0xffff0000, v154
	v_pk_fma_f32 v[218:219], v[220:221], v[210:211], v[218:219] neg_lo:[1,0,0] neg_hi:[1,0,0]
	v_lshlrev_b32_e32 v220, 16, v155
	v_and_b32_e32 v221, 0xffff0000, v155
	v_pk_fma_f32 v[218:219], v[220:221], v[212:213], v[218:219] neg_lo:[1,0,0] neg_hi:[1,0,0]
	v_lshlrev_b32_e32 v220, 16, v156
	v_and_b32_e32 v221, 0xffff0000, v156
	v_pk_fma_f32 v[218:219], v[220:221], v[214:215], v[218:219] neg_lo:[1,0,0] neg_hi:[1,0,0]
	v_lshlrev_b32_e32 v220, 16, v157
	v_fma_f32 v218, -v220, v216, v218
	v_add_f32_e32 v217, v218, v219
	v_cvt_pk_bf16_f32 v224, v217, v217
	ds_write_b16 v223, v224 offset:55776
	s_waitcnt vmcnt(17)
; #define LAS __attribute__((address_space(3)))
; __device__ __forceinline__ u32x2 cvt4(f32x4 v) { return (u32x2){pk2(v[0], v[1]), pk2(v[2], v[3])}; }
; __device__ __forceinline__ void gdn_s23(CArgs& a, int u, const GdnIn2& in, LAS unsigned char* ub, LAS unsigned char* dwb, int w, int lane, float cl) {
;     ...
;     asm volatile("s_waitcnt lgkmcnt(0)" ::: "memory");
;     f32x4 X[4];
; #pragma unroll
;     for (int I = 0; I < 4; ++I) {
;         const f32x4 br = *(const LAS f32x4*)(GT + 16 * I + 4 * kg), er = *(const LAS f32x4*)(GT + 128 + 16 * I + 4 * kg);
;         const f32x4 Rf = (f32x4){__uint_as_float(in.R[I].x << 16), __uint_as_float(in.R[I].y << 16), __uint_as_float(in.R[I].z << 16), __uint_as_float(in.R[I].w << 16)};
;         f32x4 acc = isW ? br * er * Rf : br * Rf;
; #pragma unroll
;         for (int P = 0; 2 * P < I; ++P) {
;             const u32x2 alo = *(const LAS u32x2*)(AB + (16 * I + fr) * 72 + 32 * P + 4 * kg);
;             const u32x2 ahi = (2 * P + 1 < I) ? *(const LAS u32x2*)(AB + (16 * I + fr) * 72 + 32 * P + 16 + 4 * kg) : (u32x2){0u, 0u};
;             const u32x2 xlo = cvt4(-X[2 * P]); const u32x2 xhi = (2 * P + 1 < I) ? cvt4(-X[2 * P + 1]) : (u32x2){0u, 0u};
;             acc = __builtin_amdgcn_mfma_f32_16x16x32_bf16(frag2(alo, ahi), frag2(xlo, xhi), acc, 0, 0, 0); }
;         const u32x2 dlo = *(const LAS u32x2*)(DW + (I * 16 + fr) * 16 + 4 * kg);
;         X[I] = __builtin_amdgcn_mfma_f32_16x16x32_bf16(frag2(dlo, (u32x2){0u, 0u}), frag2(cvt4(acc), (u32x2){0u, 0u}), (f32x4){0.f, 0.f, 0.f, 0.f}, 0, 0, 0);
;     }
	v_lshlrev_b32_e32 v151, 16, v151
	v_lshlrev_b32_e32 v150, 16, v150
	v_lshlrev_b32_e32 v153, 16, v153
	v_lshlrev_b32_e32 v152, 16, v152
	v_lshlrev_b32_e32 v147, 16, v147
	v_lshlrev_b32_e32 v146, 16, v146
	v_lshlrev_b32_e32 v149, 16, v149
	v_lshlrev_b32_e32 v148, 16, v148
	v_lshlrev_b32_e32 v144, 16, v144
	v_lshlrev_b32_e32 v142, 16, v142
	v_lshlrev_b32_e32 v145, 16, v145
	v_lshlrev_b32_e32 v143, 16, v143
	v_lshlrev_b32_e32 v140, 16, v140
	v_lshlrev_b32_e32 v138, 16, v138
	v_lshlrev_b32_e32 v141, 16, v141
	v_lshlrev_b32_e32 v139, 16, v139
	s_waitcnt lgkmcnt(0)
	v_add_u32_e32 v157, s8, v85
	ds_read_b128 v[94:97], v157 offset:57344
	ds_read_b128 v[86:89], v157 offset:57856
	v_ashrrev_i32_e32 v123, 4, v110
	v_lshlrev_b32_e32 v104, 3, v123
	v_lshlrev_b32_e32 v33, 16, v82
	v_lshlrev_b32_e32 v82, 16, v83
	v_lshlrev_b32_e32 v83, 16, v84
	s_waitcnt lgkmcnt(0)
	v_pk_mul_f32 v[84:85], v[96:97], v[88:89]
	v_pk_mul_f32 v[98:99], v[94:95], v[86:87]
	v_sub_u32_e32 v158, v157, v104
	v_lshlrev_b32_e32 v32, 16, v34
	v_cndmask_b32_e64 v85, v97, v85, s[38:39]
	v_cndmask_b32_e64 v84, v96, v84, s[38:39]
	v_cndmask_b32_e64 v95, v95, v99, s[38:39]
	v_cndmask_b32_e64 v94, v94, v98, s[38:39]
	v_pk_mul_f32 v[84:85], v[84:85], v[82:83]
	v_pk_mul_f32 v[82:83], v[94:95], v[32:33]
	v_lshl_add_u32 v32, v119, 5, v158
	ds_read_b64 v[32:33], v32 offset:55296
	v_cvt_pk_bf16_f32 v82, v82, v82
	v_bfe_u32 v94, v83, 16, 1
	v_mov_b32_e32 v34, v35
	v_lshrrev_b32_e32 v82, 16, v82
	v_add3_u32 v83, v83, v94, s81
	v_and_or_b32 v82, v83, s80, v82
	v_cvt_pk_bf16_f32 v83, v84, v85
	v_mov_b32_e32 v84, v35
	v_mov_b32_e32 v85, v35
	v_or_b32_e32 v156, 16, v119
	v_add_u32_e32 v154, 0, v104
	s_waitcnt lgkmcnt(0)
	v_mfma_f32_16x16x32_bf16 v[94:97], v[32:35], v[82:85], 0
	ds_read_b128 v[98:101], v157 offset:57408
	ds_read_b128 v[82:85], v157 offset:57920
	v_lshlrev_b32_e32 v32, 16, v78
	s_waitcnt vmcnt(27)
	v_lshlrev_b32_e32 v33, 16, v79
	s_waitcnt vmcnt(26)
	v_lshlrev_b32_e32 v78, 16, v80
	s_waitcnt vmcnt(25)
	v_lshlrev_b32_e32 v79, 16, v81
	s_waitcnt lgkmcnt(0)
	v_pk_mul_f32 v[80:81], v[100:101], v[84:85]
	v_pk_mul_f32 v[102:103], v[98:99], v[82:83]
	v_cndmask_b32_e64 v81, v101, v81, s[38:39]
	v_cndmask_b32_e64 v80, v100, v80, s[38:39]
	v_cndmask_b32_e64 v99, v99, v103, s[38:39]
	v_cndmask_b32_e64 v98, v98, v102, s[38:39]
	v_xor_b32_e32 v100, 0x80000000, v95
	v_pk_mul_f32 v[80:81], v[80:81], v[78:79]
	v_pk_mul_f32 v[78:79], v[98:99], v[32:33]
	v_xor_b32_e32 v99, 0x80000000, v94
	v_bfe_u32 v101, v100, 16, 1
	v_add3_u32 v100, v100, v101, s81
	v_bfe_u32 v101, v99, 16, 1
	v_add3_u32 v99, v99, v101, s81
	v_mad_u32_u24 v159, v156, s75, v154
	v_xor_b32_e32 v98, 0x80000000, v97
	v_lshrrev_b32_e32 v99, 16, v99
	ds_read_b64 v[32:33], v159
	v_xor_b32_e32 v34, 0x80000000, v96
	v_and_or_b32 v106, v100, s80, v99
	v_cvt_pk_bf16_f32 v98, v98, v98
	v_bfe_u32 v99, v34, 16, 1
	v_add3_u32 v34, v34, v99, s81
	v_lshrrev_b32_e32 v34, 16, v34
	v_and_or_b32 v107, v98, s80, v34
	v_mov_b32_e32 v34, v35
	v_mov_b32_e32 v108, v35
	v_mov_b32_e32 v109, v35
	v_or_b32_e32 v155, 32, v119
	s_ashr_i32 s27, s26, 31
	s_waitcnt lgkmcnt(0)
	v_mfma_f32_16x16x32_bf16 v[78:81], v[32:35], v[106:109], v[78:81]
	v_lshl_add_u32 v32, v156, 5, v158
	ds_read_b64 v[32:33], v32 offset:55296
	s_lshl_b64 s[76:77], s[26:27], 13
	s_add_u32 s62, s85, s76
	s_addc_u32 s63, s64, s77
	s_nop 2
	v_cvt_pk_bf16_f32 v78, v78, v78
	v_bfe_u32 v98, v79, 16, 1
	v_lshrrev_b32_e32 v78, 16, v78
	v_add3_u32 v79, v79, v98, s81
	v_and_or_b32 v78, v79, s80, v78
	v_cvt_pk_bf16_f32 v79, v80, v81
	v_mov_b32_e32 v80, v35
	v_mov_b32_e32 v81, v35
	s_add_u32 s48, s71, s76
	s_addc_u32 s49, s18, s77
	s_waitcnt lgkmcnt(0)
	v_mfma_f32_16x16x32_bf16 v[98:101], v[32:35], v[78:81], 0
	ds_read_b128 v[102:105], v157 offset:57472
	ds_read_b128 v[78:81], v157 offset:57984
	s_waitcnt vmcnt(24)
	v_lshlrev_b32_e32 v32, 16, v90
	s_waitcnt vmcnt(23)
	v_lshlrev_b32_e32 v33, 16, v91
	s_waitcnt vmcnt(22)
	v_lshlrev_b32_e32 v90, 16, v92
	s_waitcnt vmcnt(21)
	v_lshlrev_b32_e32 v91, 16, v93
	s_waitcnt lgkmcnt(0)
	v_pk_mul_f32 v[92:93], v[104:105], v[80:81]
	v_pk_mul_f32 v[108:109], v[102:103], v[78:79]
	v_cndmask_b32_e64 v93, v105, v93, s[38:39]
	v_cndmask_b32_e64 v92, v104, v92, s[38:39]
	v_cndmask_b32_e64 v103, v103, v109, s[38:39]
	v_cndmask_b32_e64 v102, v102, v108, s[38:39]
	v_pk_mul_f32 v[92:93], v[92:93], v[90:91]
	v_pk_mul_f32 v[90:91], v[102:103], v[32:33]
	v_add_u32_e32 v32, 0x800, v159
	v_xor_b32_e32 v108, 0x80000000, v99
	ds_read2_b64 v[102:105], v32 offset0:32 offset1:36
	v_xor_b32_e32 v34, 0x80000000, v98
	v_xor_b32_e32 v33, 0x80000000, v101
	v_xor_b32_e32 v32, 0x80000000, v100
	v_cvt_pk_bf16_f32 v108, v34, v108
	v_cvt_pk_bf16_f32 v109, v32, v33
	v_lshl_add_u32 v32, v155, 5, v158
	ds_read_b64 v[32:33], v32 offset:55296
	s_waitcnt lgkmcnt(1)
; #define LAS __attribute__((address_space(3)))
; __device__ __forceinline__ u32x2 cvt4(f32x4 v) { return (u32x2){pk2(v[0], v[1]), pk2(v[2], v[3])}; }
; __device__ __forceinline__ void gdn_s23(CArgs& a, int u, const GdnIn2& in, LAS unsigned char* ub, LAS unsigned char* dwb, int w, int lane, float cl) {
;     ...
;     const bf16x8 Xb01 = frag2(cvt4(X[0]), cvt4(X[1])), Xb23 = frag2(cvt4(X[2]), cvt4(X[3]));
;     const float ecl = __expf(cl);
;     bf16* ftp = FTo + (c0 + fr) * 64 + 4 * kg; bf16* btp = BTo + (c0 + fr) * 64 + 4 * kg; bf16* ep = Eo + (4 * kg) * 64 + c0 + fr; bf16* mp = Mo + (4 * kg) * 64 + c0 + fr;
; #pragma unroll
;     for (int t4 = 0; t4 < 4; ++t4) {
;         const LAS bf16* ar = ATT + (16 * t4 + fr) * 72 + 4 * kg; const LAS bf16* kr = KTT + (16 * t4 + fr) * 72 + 4 * kg;
;         f32x4 pa = (f32x4){0.f, 0.f, 0.f, 0.f}, pk = (f32x4){0.f, 0.f, 0.f, 0.f};
;         pa = __builtin_amdgcn_mfma_f32_16x16x32_bf16(frag2(*(const LAS u32x2*)ar, *(const LAS u32x2*)(ar + 16)), Xb01, pa, 0, 0, 0);
;         pa = __builtin_amdgcn_mfma_f32_16x16x32_bf16(frag2(*(const LAS u32x2*)(ar + 32), *(const LAS u32x2*)(ar + 48)), Xb23, pa, 0, 0, 0);
;         pk = __builtin_amdgcn_mfma_f32_16x16x32_bf16(frag2(*(const LAS u32x2*)kr, *(const LAS u32x2*)(kr + 16)), Xb01, pk, 0, 0, 0);
;         pk = __builtin_amdgcn_mfma_f32_16x16x32_bf16(frag2(*(const LAS u32x2*)(kr + 32), *(const LAS u32x2*)(kr + 48)), Xb23, pk, 0, 0, 0);
;         if (!isW) {
;             *(u32x2*)(ftp + 16 * t4) = cvt4(pa);
;             *(u32x2*)(btp + 16 * t4) = cvt4(pk);
	v_mfma_f32_16x16x32_bf16 v[90:93], v[102:105], v[106:109], v[90:93]
	v_mov_b32_e32 v34, v35
	s_add_u32 s2, s19, s76
	v_lshlrev_b32_e32 v116, 2, v123
	s_addc_u32 s3, s66, s77
	s_add_u32 s54, s21, s76
	s_nop 2
	v_cvt_pk_bf16_f32 v90, v90, v90
	v_bfe_u32 v102, v91, 16, 1
	v_lshrrev_b32_e32 v90, 16, v90
	v_add3_u32 v91, v91, v102, s81
	v_and_or_b32 v90, v91, s80, v90
	v_cvt_pk_bf16_f32 v91, v92, v93
	v_mov_b32_e32 v92, v35
	v_mov_b32_e32 v93, v35
	s_addc_u32 s55, s70, s77
	s_mov_b64 s[76:77], -1
	s_waitcnt lgkmcnt(0)
	v_mfma_f32_16x16x32_bf16 v[102:105], v[32:35], v[90:93], 0
	ds_read_b128 v[170:173], v157 offset:57536
	ds_read_b128 v[90:93], v157 offset:58048
	s_waitcnt vmcnt(20)
	v_lshlrev_b32_e32 v32, 16, v117
	s_waitcnt vmcnt(19)
	v_lshlrev_b32_e32 v33, 16, v120
	s_waitcnt vmcnt(18)
	v_lshlrev_b32_e32 v120, 16, v121
	s_waitcnt vmcnt(17)
	v_lshlrev_b32_e32 v121, 16, v122
	s_waitcnt lgkmcnt(0)
	v_pk_mul_f32 v[174:175], v[170:171], v[90:91]
	v_pk_mul_f32 v[162:163], v[172:173], v[92:93]
	v_cndmask_b32_e64 v171, v171, v175, s[38:39]
	v_cndmask_b32_e64 v170, v170, v174, s[38:39]
	v_pk_mul_f32 v[170:171], v[170:171], v[32:33]
	v_add_u32_e32 v32, 0x1000, v159
	ds_read2_b64 v[174:177], v32 offset0:64 offset1:68
	v_cndmask_b32_e64 v163, v173, v163, s[38:39]
	v_cndmask_b32_e64 v162, v172, v162, s[38:39]
	v_pk_mul_f32 v[172:173], v[162:163], v[120:121]
	v_xor_b32_e32 v121, 0x80000000, v103
	v_xor_b32_e32 v120, 0x80000000, v102
	v_cvt_pk_bf16_f32 v121, v121, v121
	v_cvt_pk_bf16_f32 v120, v120, v120
	v_xor_b32_e32 v117, 0x80000000, v105
	v_lshrrev_b32_e32 v120, 16, v120
	s_waitcnt lgkmcnt(0)
	v_mfma_f32_16x16x32_bf16 v[106:109], v[174:177], v[106:109], v[170:173]
	ds_read_b64 v[32:33], v159 offset:4672
	v_xor_b32_e32 v34, 0x80000000, v104
	v_or_b32_e32 v157, 48, v119
	v_and_or_b32 v170, v121, s80, v120
	v_cvt_pk_bf16_f32 v171, v34, v117
	v_mov_b32_e32 v34, v35
	v_mov_b32_e32 v172, v35
	v_mov_b32_e32 v173, v35
	s_andn2_b64 vcc, exec, s[60:61]
	s_waitcnt lgkmcnt(0)
	v_mfma_f32_16x16x32_bf16 v[106:109], v[32:35], v[170:173], v[106:109]
	v_lshl_add_u32 v32, v157, 5, v158
	ds_read_b64 v[32:33], v32 offset:55296
	s_nop 5
	v_cvt_pk_bf16_f32 v106, v106, v107
	v_cvt_pk_bf16_f32 v107, v108, v109
	v_mov_b32_e32 v108, v35
	v_mov_b32_e32 v109, v35
	v_ashrrev_i32_e32 v117, 31, v116
	s_waitcnt lgkmcnt(0)
	v_mfma_f32_16x16x32_bf16 v[106:109], v[32:35], v[106:109], 0
	v_cvt_pk_bf16_f32 v94, v94, v95
	v_cvt_pk_bf16_f32 v95, v96, v97
	v_cvt_pk_bf16_f32 v96, v98, v99
	v_cvt_pk_bf16_f32 v97, v100, v101
	v_cvt_pk_bf16_f32 v98, v102, v103
	v_cvt_pk_bf16_f32 v99, v104, v105
	s_nop 1
	v_cvt_pk_bf16_f32 v100, v106, v107
	v_lshlrev_b32_e32 v34, 7, v45
	v_cvt_pk_bf16_f32 v101, v108, v109
	v_lshl_add_u64 v[32:33], s[48:49], 0, v[34:35]
	v_lshlrev_b64 v[102:103], 1, v[116:117]
	v_lshl_add_u64 v[120:121], v[32:33], 0, v[102:103]
	v_lshl_add_u64 v[32:33], s[54:55], 0, v[34:35]
	v_mul_u32_u24_e32 v34, 0x48, v119
	v_lshl_add_u32 v34, v34, 1, v154
	v_add_u32_e32 v106, 0x2000, v34
	v_lshl_add_u64 v[32:33], v[32:33], 0, v[102:103]
	ds_read2_b64 v[102:105], v106 offset0:128 offset1:132
	ds_read2_b64 v[106:109], v106 offset0:136 offset1:140
	s_waitcnt lgkmcnt(1)
	v_mfma_f32_16x16x32_bf16 v[102:105], v[102:105], v[94:97], 0
	v_add_u32_e32 v34, 0x4800, v34
	ds_read2_b64 v[170:173], v34 offset0:8 offset1:12
	s_waitcnt lgkmcnt(1)
	v_mfma_f32_16x16x32_bf16 v[102:105], v[106:109], v[98:101], v[102:105]
	ds_read2_b64 v[106:109], v34 offset1:4
	v_cndmask_b32_e64 v34, 0, 1, s[60:61]
	v_cmp_ne_u32_e64 s[48:49], 1, v34
	s_waitcnt lgkmcnt(0)
	v_mfma_f32_16x16x32_bf16 v[106:109], v[106:109], v[94:97], 0
	v_mfma_f32_16x16x32_bf16 v[106:109], v[170:173], v[98:101], v[106:109]
	v_mul_u32_u24_e32 v218, 0x48, v156
	v_lshl_add_u32 v218, v218, 1, v154
	v_add_u32_e32 v219, 0x2000, v218
	v_add_u32_e32 v218, 0x4800, v218
	ds_read2_b64 v[202:205], v219 offset0:128 offset1:132
	ds_read2_b64 v[206:209], v219 offset0:136 offset1:140
	ds_read2_b64 v[210:213], v218 offset1:4
	ds_read2_b64 v[214:217], v218 offset0:8 offset1:12
	s_cbranch_vccnz .LBB0_1725
	s_nop 0
	v_cvt_pk_bf16_f32 v158, v102, v103
	v_cvt_pk_bf16_f32 v159, v104, v105
	global_store_dwordx2 v[120:121], v[158:159], off
	s_nop 2
	v_cvt_pk_bf16_f32 v158, v106, v107
	v_cvt_pk_bf16_f32 v34, v108, v108
	v_bfe_u32 v117, v109, 16, 1
	v_lshrrev_b32_e32 v34, 16, v34
	v_add3_u32 v117, v109, v117, s81
	v_and_or_b32 v159, v117, s80, v34
	s_mov_b64 s[76:77], 0
	global_store_dwordx2 v[32:33], v[158:159], off

; #define LAS __attribute__((address_space(3)))
; __device__ __forceinline__ u32x2 cvt4(f32x4 v) { return (u32x2){pk2(v[0], v[1]), pk2(v[2], v[3])}; }
; __device__ __forceinline__ void gdn_s23(CArgs& a, int u, const GdnIn2& in, LAS unsigned char* ub, LAS unsigned char* dwb, int w, int lane, float cl) {
;     ...
;     for (int t4 = 0; t4 < 4; ++t4) {
;         const LAS bf16* ar = ATT + (16 * t4 + fr) * 72 + 4 * kg; const LAS bf16* kr = KTT + (16 * t4 + fr) * 72 + 4 * kg;
;         f32x4 pa = (f32x4){0.f, 0.f, 0.f, 0.f}, pk = (f32x4){0.f, 0.f, 0.f, 0.f};
;         pa = __builtin_amdgcn_mfma_f32_16x16x32_bf16(frag2(*(const LAS u32x2*)ar, *(const LAS u32x2*)(ar + 16)), Xb01, pa, 0, 0, 0);
;         pa = __builtin_amdgcn_mfma_f32_16x16x32_bf16(frag2(*(const LAS u32x2*)(ar + 32), *(const LAS u32x2*)(ar + 48)), Xb23, pa, 0, 0, 0);
;         pk = __builtin_amdgcn_mfma_f32_16x16x32_bf16(frag2(*(const LAS u32x2*)kr, *(const LAS u32x2*)(kr + 16)), Xb01, pk, 0, 0, 0);
;         pk = __builtin_amdgcn_mfma_f32_16x16x32_bf16(frag2(*(const LAS u32x2*)(kr + 32), *(const LAS u32x2*)(kr + 48)), Xb23, pk, 0, 0, 0);
;         if (!isW) {
;             *(u32x2*)(ftp + 16 * t4) = cvt4(pa);
;             *(u32x2*)(btp + 16 * t4) = cvt4(pk);
.LBB0_1727:
	s_mov_b64 s[2:3], -1
	s_and_b64 vcc, exec, s[48:49]
	s_waitcnt lgkmcnt(0)
	v_mfma_f32_16x16x32_bf16 v[86:89], v[202:205], v[94:97], 0
	v_mfma_f32_16x16x32_bf16 v[86:89], v[206:209], v[98:101], v[86:89]
	v_mfma_f32_16x16x32_bf16 v[102:105], v[210:213], v[94:97], 0
	v_mfma_f32_16x16x32_bf16 v[102:105], v[214:217], v[98:101], v[102:105]
	v_mul_u32_u24_e32 v218, 0x48, v155
	v_lshl_add_u32 v218, v218, 1, v154
	v_add_u32_e32 v219, 0x2000, v218
	v_add_u32_e32 v218, 0x4800, v218
	ds_read2_b64 v[226:229], v219 offset0:128 offset1:132
	ds_read2_b64 v[230:233], v219 offset0:136 offset1:140
	ds_read2_b64 v[234:237], v218 offset1:4
	ds_read2_b64 v[238:241], v218 offset0:8 offset1:12
	s_cbranch_vccnz .LBB0_1729
	s_nop 0
	v_cvt_pk_bf16_f32 v106, v86, v87
	v_cvt_pk_bf16_f32 v107, v88, v89
	global_store_dwordx2 v[120:121], v[106:107], off offset:32
	s_nop 2
	v_cvt_pk_bf16_f32 v106, v102, v103
	v_cvt_pk_bf16_f32 v107, v104, v104
	v_bfe_u32 v108, v105, 16, 1
	v_lshrrev_b32_e32 v107, 16, v107
	v_add3_u32 v108, v105, v108, s81
	v_and_or_b32 v107, v108, s80, v107
	s_mov_b64 s[2:3], 0
	global_store_dwordx2 v[32:33], v[106:107], off offset:32

; #define LAS __attribute__((address_space(3)))
; __device__ __forceinline__ u32x2 cvt4(f32x4 v) { return (u32x2){pk2(v[0], v[1]), pk2(v[2], v[3])}; }
; __device__ __forceinline__ void gdn_s23(CArgs& a, int u, const GdnIn2& in, LAS unsigned char* ub, LAS unsigned char* dwb, int w, int lane, float cl) {
;     ...
;     for (int t4 = 0; t4 < 4; ++t4) {
;         const LAS bf16* ar = ATT + (16 * t4 + fr) * 72 + 4 * kg; const LAS bf16* kr = KTT + (16 * t4 + fr) * 72 + 4 * kg;
;         f32x4 pa = (f32x4){0.f, 0.f, 0.f, 0.f}, pk = (f32x4){0.f, 0.f, 0.f, 0.f};
;         pa = __builtin_amdgcn_mfma_f32_16x16x32_bf16(frag2(*(const LAS u32x2*)ar, *(const LAS u32x2*)(ar + 16)), Xb01, pa, 0, 0, 0);
;         pa = __builtin_amdgcn_mfma_f32_16x16x32_bf16(frag2(*(const LAS u32x2*)(ar + 32), *(const LAS u32x2*)(ar + 48)), Xb23, pa, 0, 0, 0);
;         pk = __builtin_amdgcn_mfma_f32_16x16x32_bf16(frag2(*(const LAS u32x2*)kr, *(const LAS u32x2*)(kr + 16)), Xb01, pk, 0, 0, 0);
;         pk = __builtin_amdgcn_mfma_f32_16x16x32_bf16(frag2(*(const LAS u32x2*)(kr + 32), *(const LAS u32x2*)(kr + 48)), Xb23, pk, 0, 0, 0);
;         if (!isW) {
;             *(u32x2*)(ftp + 16 * t4) = cvt4(pa);
;             *(u32x2*)(btp + 16 * t4) = cvt4(pk);
.LBB0_1731:
	s_mov_b64 s[2:3], -1
	s_and_b64 vcc, exec, s[48:49]
	s_waitcnt lgkmcnt(0)
	v_mfma_f32_16x16x32_bf16 v[82:85], v[226:229], v[94:97], 0
	v_mfma_f32_16x16x32_bf16 v[82:85], v[230:233], v[98:101], v[82:85]
	v_mfma_f32_16x16x32_bf16 v[86:89], v[234:237], v[94:97], 0
	v_mfma_f32_16x16x32_bf16 v[86:89], v[238:241], v[98:101], v[86:89]
	v_mul_u32_u24_e32 v218, 0x48, v157
	v_lshl_add_u32 v218, v218, 1, v154
	v_add_u32_e32 v219, 0x2000, v218
	v_add_u32_e32 v218, 0x4800, v218
	ds_read2_b64 v[202:205], v219 offset0:128 offset1:132
	ds_read2_b64 v[206:209], v219 offset0:136 offset1:140
	ds_read2_b64 v[210:213], v218 offset1:4
	ds_read2_b64 v[214:217], v218 offset0:8 offset1:12
	s_cbranch_vccnz .LBB0_1733
	s_nop 0
	v_cvt_pk_bf16_f32 v102, v82, v83
	v_cvt_pk_bf16_f32 v103, v84, v85
	global_store_dwordx2 v[120:121], v[102:103], off offset:64
	s_nop 2
	v_cvt_pk_bf16_f32 v102, v86, v87
	v_cvt_pk_bf16_f32 v103, v88, v88
	v_bfe_u32 v104, v89, 16, 1
	v_lshrrev_b32_e32 v103, 16, v103
	v_add3_u32 v104, v89, v104, s81
	v_and_or_b32 v103, v104, s80, v103
	s_mov_b64 s[2:3], 0
	global_store_dwordx2 v[32:33], v[102:103], off offset:64

; #define LAS __attribute__((address_space(3)))
; __device__ __forceinline__ u32x2 cvt4(f32x4 v) { return (u32x2){pk2(v[0], v[1]), pk2(v[2], v[3])}; }
; __device__ __forceinline__ void gdn_s23(CArgs& a, int u, const GdnIn2& in, LAS unsigned char* ub, LAS unsigned char* dwb, int w, int lane, float cl) {
;     ...
;     for (int t4 = 0; t4 < 4; ++t4) {
;         const LAS bf16* ar = ATT + (16 * t4 + fr) * 72 + 4 * kg; const LAS bf16* kr = KTT + (16 * t4 + fr) * 72 + 4 * kg;
;         f32x4 pa = (f32x4){0.f, 0.f, 0.f, 0.f}, pk = (f32x4){0.f, 0.f, 0.f, 0.f};
;         pa = __builtin_amdgcn_mfma_f32_16x16x32_bf16(frag2(*(const LAS u32x2*)ar, *(const LAS u32x2*)(ar + 16)), Xb01, pa, 0, 0, 0);
;         pa = __builtin_amdgcn_mfma_f32_16x16x32_bf16(frag2(*(const LAS u32x2*)(ar + 32), *(const LAS u32x2*)(ar + 48)), Xb23, pa, 0, 0, 0);
;         pk = __builtin_amdgcn_mfma_f32_16x16x32_bf16(frag2(*(const LAS u32x2*)kr, *(const LAS u32x2*)(kr + 16)), Xb01, pk, 0, 0, 0);
;         pk = __builtin_amdgcn_mfma_f32_16x16x32_bf16(frag2(*(const LAS u32x2*)(kr + 32), *(const LAS u32x2*)(kr + 48)), Xb23, pk, 0, 0, 0);
;         if (!isW) {
;             *(u32x2*)(ftp + 16 * t4) = cvt4(pa);
;             *(u32x2*)(btp + 16 * t4) = cvt4(pk);
.LBB0_1735:
	s_mov_b64 s[2:3], -1
	s_and_b64 vcc, exec, s[48:49]
	s_waitcnt lgkmcnt(0)
	v_mfma_f32_16x16x32_bf16 v[78:81], v[202:205], v[94:97], 0
	v_mfma_f32_16x16x32_bf16 v[78:81], v[206:209], v[98:101], v[78:81]
	v_mfma_f32_16x16x32_bf16 v[82:85], v[210:213], v[94:97], 0
	v_mfma_f32_16x16x32_bf16 v[82:85], v[214:217], v[98:101], v[82:85]
	s_cbranch_vccnz .LBB0_1737
	s_nop 0
	s_nop 3
	v_cvt_pk_bf16_f32 v86, v78, v79
	v_cvt_pk_bf16_f32 v87, v80, v81
	global_store_dwordx2 v[120:121], v[86:87], off offset:96
	s_nop 2
	v_cvt_pk_bf16_f32 v86, v82, v83
	v_cvt_pk_bf16_f32 v87, v84, v84
	v_bfe_u32 v88, v85, 16, 1
	v_lshrrev_b32_e32 v87, 16, v87
	v_add3_u32 v88, v85, v88, s81
	v_and_or_b32 v87, v88, s80, v87
	s_mov_b64 s[2:3], 0
	global_store_dwordx2 v[32:33], v[86:87], off offset:96

; #define LAS __attribute__((address_space(3)))
; __device__ __forceinline__ u32x2 cvt4(f32x4 v) { return (u32x2){pk2(v[0], v[1]), pk2(v[2], v[3])}; }
; __device__ __forceinline__ void gdn_s23(CArgs& a, int u, const GdnIn2& in, LAS unsigned char* ub, LAS unsigned char* dwb, int w, int lane, float cl) {
;     ...
;     asm volatile("s_waitcnt lgkmcnt(0)" ::: "memory");
;     f32x4 X[4];
; #pragma unroll
;     for (int I = 0; I < 4; ++I) {
;         const f32x4 br = *(const LAS f32x4*)(GT + 16 * I + 4 * kg), er = *(const LAS f32x4*)(GT + 128 + 16 * I + 4 * kg);
;         const f32x4 Rf = (f32x4){__uint_as_float(in.R[I].x << 16), __uint_as_float(in.R[I].y << 16), __uint_as_float(in.R[I].z << 16), __uint_as_float(in.R[I].w << 16)};
;         f32x4 acc = isW ? br * er * Rf : br * Rf;
; #pragma unroll
;         for (int P = 0; 2 * P < I; ++P) {
;             const u32x2 alo = *(const LAS u32x2*)(AB + (16 * I + fr) * 72 + 32 * P + 4 * kg);
;             const u32x2 ahi = (2 * P + 1 < I) ? *(const LAS u32x2*)(AB + (16 * I + fr) * 72 + 32 * P + 16 + 4 * kg) : (u32x2){0u, 0u};
;             const u32x2 xlo = cvt4(-X[2 * P]); const u32x2 xhi = (2 * P + 1 < I) ? cvt4(-X[2 * P + 1]) : (u32x2){0u, 0u};
;             acc = __builtin_amdgcn_mfma_f32_16x16x32_bf16(frag2(alo, ahi), frag2(xlo, xhi), acc, 0, 0, 0); }
;         const u32x2 dlo = *(const LAS u32x2*)(DW + (I * 16 + fr) * 16 + 4 * kg);
;         X[I] = __builtin_amdgcn_mfma_f32_16x16x32_bf16(frag2(dlo, (u32x2){0u, 0u}), frag2(cvt4(acc), (u32x2){0u, 0u}), (f32x4){0.f, 0.f, 0.f, 0.f}, 0, 0, 0);
;     }
.Lgdf_j:
	v_lshlrev_b32_e32 v103, 16, v103
	v_lshlrev_b32_e32 v102, 16, v102
	v_lshlrev_b32_e32 v105, 16, v105
	v_lshlrev_b32_e32 v104, 16, v104
	v_lshlrev_b32_e32 v99, 16, v99
	v_lshlrev_b32_e32 v98, 16, v98
	v_lshlrev_b32_e32 v101, 16, v101
	v_lshlrev_b32_e32 v100, 16, v100
	v_lshlrev_b32_e32 v96, 16, v96
	v_lshlrev_b32_e32 v94, 16, v94
	v_lshlrev_b32_e32 v97, 16, v97
	v_lshlrev_b32_e32 v95, 16, v95
	v_lshlrev_b32_e32 v92, 16, v92
	v_lshlrev_b32_e32 v90, 16, v90
	v_lshlrev_b32_e32 v93, 16, v93
	v_lshlrev_b32_e32 v91, 16, v91
	s_waitcnt lgkmcnt(0)
	v_add_u32_e32 v79, s8, v76
	ds_read_b128 v[46:49], v79 offset:57344
	ds_read_b128 v[54:57], v79 offset:57856
	v_lshlrev_b32_e32 v70, 3, v82
	v_sub_u32_e32 v33, v79, v70
	s_waitcnt vmcnt(15)
	v_lshlrev_b32_e32 v50, 16, v123
	s_waitcnt vmcnt(14)
	v_lshlrev_b32_e32 v51, 16, v139
	s_waitcnt lgkmcnt(0)
	v_pk_mul_f32 v[60:61], v[46:47], v[54:55]
	v_pk_mul_f32 v[58:59], v[48:49], v[56:57]
	v_cndmask_b32_e64 v47, v47, v61, s[38:39]
	v_cndmask_b32_e64 v46, v46, v60, s[38:39]
	v_pk_mul_f32 v[50:51], v[46:47], v[50:51]
	v_lshl_add_u32 v46, v106, 5, v33
	ds_read_b64 v[46:47], v46 offset:55296
	v_cndmask_b32_e64 v48, v48, v58, s[38:39]
	s_waitcnt vmcnt(13)
	v_lshlrev_b32_e32 v52, 16, v141
	s_waitcnt vmcnt(12)
	v_lshlrev_b32_e32 v53, 16, v142
	v_cndmask_b32_e64 v49, v49, v59, s[38:39]
	v_pk_mul_f32 v[52:53], v[48:49], v[52:53]
	v_mov_b32_e32 v48, v35
	v_mov_b32_e32 v49, v35
	v_cvt_pk_bf16_f32 v50, v50, v51
	v_cvt_pk_bf16_f32 v51, v52, v53
	v_mov_b32_e32 v52, v35
	v_mov_b32_e32 v53, v35
	s_waitcnt vmcnt(9)
	v_lshlrev_b32_e32 v60, 16, v138
	s_waitcnt vmcnt(8)
	v_lshlrev_b32_e32 v61, 16, v140
	s_waitcnt lgkmcnt(0)
	v_mfma_f32_16x16x32_bf16 v[62:65], v[46:49], v[50:53], 0
	ds_read_b128 v[46:49], v79 offset:57408
	ds_read_b128 v[50:53], v79 offset:57920
	v_or_b32_e32 v89, 16, v106
	v_add_u32_e32 v86, 0, v70
	v_lshlrev_b32_e32 v58, 16, v121
	v_lshlrev_b32_e32 v59, 16, v122
	s_waitcnt lgkmcnt(0)
	v_pk_mul_f32 v[66:67], v[48:49], v[52:53]
	v_pk_mul_f32 v[68:69], v[46:47], v[50:51]
	v_cndmask_b32_e64 v49, v49, v67, s[38:39]
	v_xor_b32_e32 v67, 0x80000000, v63
	v_cndmask_b32_e64 v48, v48, v66, s[38:39]
	v_cndmask_b32_e64 v46, v46, v68, s[38:39]
	v_xor_b32_e32 v66, 0x80000000, v62
	v_bfe_u32 v68, v67, 16, 1
	v_add3_u32 v67, v67, v68, s81
	v_bfe_u32 v68, v66, 16, 1
	v_add3_u32 v66, v66, v68, s81
	v_cndmask_b32_e64 v47, v47, v69, s[38:39]
	v_pk_mul_f32 v[48:49], v[48:49], v[60:61]
	v_mad_u32_u24 v78, v89, s75, v86
	v_xor_b32_e32 v61, 0x80000000, v65
	v_lshrrev_b32_e32 v66, 16, v66
	v_pk_mul_f32 v[46:47], v[46:47], v[58:59]
	ds_read_b64 v[58:59], v78 offset:27648
	v_xor_b32_e32 v60, 0x80000000, v64
	v_and_or_b32 v74, v67, s80, v66
	v_cvt_pk_bf16_f32 v75, v60, v61
	v_mov_b32_e32 v60, v35
	v_mov_b32_e32 v61, v35
	v_mov_b32_e32 v76, v35
	v_mov_b32_e32 v77, v35
	s_waitcnt vmcnt(7)
	v_lshlrev_b32_e32 v70, 16, v107
	s_waitcnt vmcnt(6)
	v_lshlrev_b32_e32 v71, 16, v108
	s_waitcnt lgkmcnt(0)
	v_mfma_f32_16x16x32_bf16 v[46:49], v[58:61], v[74:77], v[46:49]
	v_lshl_add_u32 v58, v89, 5, v33
	ds_read_b64 v[58:59], v58 offset:55296
	s_waitcnt vmcnt(5)
	v_lshlrev_b32_e32 v72, 16, v109
	s_waitcnt vmcnt(4)
	v_lshlrev_b32_e32 v73, 16, v117
	v_or_b32_e32 v88, 32, v106
	s_nop 0
	v_cvt_pk_bf16_f32 v46, v46, v46
	v_bfe_u32 v66, v47, 16, 1
	v_lshrrev_b32_e32 v46, 16, v46
	v_add3_u32 v47, v47, v66, s81
	v_and_or_b32 v46, v47, s80, v46
	v_cvt_pk_bf16_f32 v47, v48, v49
	v_mov_b32_e32 v48, v35
	v_mov_b32_e32 v49, v35
	s_waitcnt vmcnt(1)
	v_lshlrev_b32_e32 v84, 16, v119
	s_waitcnt vmcnt(0)
	v_lshlrev_b32_e32 v85, 16, v120
	s_waitcnt lgkmcnt(0)
	v_mfma_f32_16x16x32_bf16 v[66:69], v[58:61], v[46:49], 0
	ds_read_b128 v[46:49], v79 offset:57472
	ds_read_b128 v[58:61], v79 offset:57984
	v_or_b32_e32 v87, 48, v106
	s_ashr_i32 s29, s28, 31
	s_lshl_b64 s[52:53], s[28:29], 13
	s_add_u32 s26, s85, s52
	s_waitcnt lgkmcnt(0)
	v_pk_mul_f32 v[80:81], v[46:47], v[58:59]
	v_pk_mul_f32 v[76:77], v[48:49], v[60:61]
	v_cndmask_b32_e64 v47, v47, v81, s[38:39]
	v_cndmask_b32_e64 v46, v46, v80, s[38:39]
	v_cndmask_b32_e64 v49, v49, v77, s[38:39]
	v_cndmask_b32_e64 v48, v48, v76, s[38:39]
	v_pk_mul_f32 v[46:47], v[46:47], v[70:71]
	v_add_u32_e32 v70, 0x7000, v78
	v_xor_b32_e32 v81, 0x80000000, v67
	v_pk_mul_f32 v[48:49], v[48:49], v[72:73]
	ds_read2_b64 v[70:73], v70 offset0:160 offset1:164
	v_xor_b32_e32 v76, 0x80000000, v66
	v_xor_b32_e32 v80, 0x80000000, v69
	v_xor_b32_e32 v77, 0x80000000, v68
	v_cvt_pk_bf16_f32 v76, v76, v81
	v_cvt_pk_bf16_f32 v77, v77, v80
	v_lshlrev_b32_e32 v81, 16, v118
	s_addc_u32 s27, s64, s53
	s_waitcnt lgkmcnt(0)
; #define LAS __attribute__((address_space(3)))
; __device__ __forceinline__ u32x2 cvt4(f32x4 v) { return (u32x2){pk2(v[0], v[1]), pk2(v[2], v[3])}; }
; __device__ __forceinline__ void gdn_s23(CArgs& a, int u, const GdnIn2& in, LAS unsigned char* ub, LAS unsigned char* dwb, int w, int lane, float cl) {
;     ...
; #pragma unroll
;         for (int P = 0; 2 * P < I; ++P) {
;             const u32x2 alo = *(const LAS u32x2*)(AB + (16 * I + fr) * 72 + 32 * P + 4 * kg);
;             const u32x2 ahi = (2 * P + 1 < I) ? *(const LAS u32x2*)(AB + (16 * I + fr) * 72 + 32 * P + 16 + 4 * kg) : (u32x2){0u, 0u};
;             const u32x2 xlo = cvt4(-X[2 * P]); const u32x2 xhi = (2 * P + 1 < I) ? cvt4(-X[2 * P + 1]) : (u32x2){0u, 0u};
;             acc = __builtin_amdgcn_mfma_f32_16x16x32_bf16(frag2(alo, ahi), frag2(xlo, xhi), acc, 0, 0, 0); }
;         const u32x2 dlo = *(const LAS u32x2*)(DW + (I * 16 + fr) * 16 + 4 * kg);
;         X[I] = __builtin_amdgcn_mfma_f32_16x16x32_bf16(frag2(dlo, (u32x2){0u, 0u}), frag2(cvt4(acc), (u32x2){0u, 0u}), (f32x4){0.f, 0.f, 0.f, 0.f}, 0, 0, 0);
;     }
;     const bf16x8 Xb01 = frag2(cvt4(X[0]), cvt4(X[1])), Xb23 = frag2(cvt4(X[2]), cvt4(X[3]));
;     const float ecl = __expf(cl);
;     bf16* ftp = FTo + (c0 + fr) * 64 + 4 * kg; bf16* btp = BTo + (c0 + fr) * 64 + 4 * kg; bf16* ep = Eo + (4 * kg) * 64 + c0 + fr; bf16* mp = Mo + (4 * kg) * 64 + c0 + fr;
; #pragma unroll
;     for (int t4 = 0; t4 < 4; ++t4) {
;         const LAS bf16* ar = ATT + (16 * t4 + fr) * 72 + 4 * kg; const LAS bf16* kr = KTT + (16 * t4 + fr) * 72 + 4 * kg;
;         f32x4 pa = (f32x4){0.f, 0.f, 0.f, 0.f}, pk = (f32x4){0.f, 0.f, 0.f, 0.f};
;         pa = __builtin_amdgcn_mfma_f32_16x16x32_bf16(frag2(*(const LAS u32x2*)ar, *(const LAS u32x2*)(ar + 16)), Xb01, pa, 0, 0, 0);
;         pa = __builtin_amdgcn_mfma_f32_16x16x32_bf16(frag2(*(const LAS u32x2*)(ar + 32), *(const LAS u32x2*)(ar + 48)), Xb23, pa, 0, 0, 0);
;         pk = __builtin_amdgcn_mfma_f32_16x16x32_bf16(frag2(*(const LAS u32x2*)kr, *(const LAS u32x2*)(kr + 16)), Xb01, pk, 0, 0, 0);
;         pk = __builtin_amdgcn_mfma_f32_16x16x32_bf16(frag2(*(const LAS u32x2*)(kr + 32), *(const LAS u32x2*)(kr + 48)), Xb23, pk, 0, 0, 0);
;         if (!isW) {
;             *(u32x2*)(ftp + 16 * t4) = cvt4(pa);
;             *(u32x2*)(btp + 16 * t4) = cvt4(pk);
	v_mfma_f32_16x16x32_bf16 v[46:49], v[70:73], v[74:77], v[46:49]
	v_lshl_add_u32 v70, v88, 5, v33
	ds_read_b64 v[70:71], v70 offset:55296
	v_mov_b32_e32 v72, v35
	v_mov_b32_e32 v73, v35
	v_lshl_add_u32 v33, v87, 5, v33
	s_nop 2
	v_cvt_pk_bf16_f32 v46, v46, v47
	v_cvt_pk_bf16_f32 v47, v48, v49
	v_mov_b32_e32 v48, v35
	v_mov_b32_e32 v49, v35
	v_lshlrev_b32_e32 v80, 16, v116
	s_add_u32 s28, s71, s52
	s_waitcnt lgkmcnt(0)
	v_mfma_f32_16x16x32_bf16 v[70:73], v[70:73], v[46:49], 0
	ds_read_b128 v[126:129], v79 offset:57536
	ds_read_b128 v[46:49], v79 offset:58048
	v_add_u32_e32 v79, 0x7800, v78
	ds_read2_b64 v[118:121], v79 offset0:192 offset1:196
	ds_read_b64 v[78:79], v78 offset:32320
	s_nop 2
	v_xor_b32_e32 v83, 0x80000000, v70
	s_waitcnt lgkmcnt(2)
	v_pk_mul_f32 v[108:109], v[128:129], v[48:49]
	v_pk_mul_f32 v[114:115], v[126:127], v[46:47]
	v_cndmask_b32_e64 v109, v129, v109, s[38:39]
	v_cndmask_b32_e64 v108, v128, v108, s[38:39]
	v_pk_mul_f32 v[116:117], v[108:109], v[84:85]
	v_xor_b32_e32 v84, 0x80000000, v71
	v_bfe_u32 v85, v84, 16, 1
	v_add3_u32 v84, v84, v85, s81
	v_cndmask_b32_e64 v115, v127, v115, s[38:39]
	v_cndmask_b32_e64 v114, v126, v114, s[38:39]
	v_cvt_pk_bf16_f32 v83, v83, v83
	v_pk_mul_f32 v[114:115], v[114:115], v[80:81]
	v_xor_b32_e32 v81, 0x80000000, v73
	v_lshrrev_b32_e32 v83, 16, v83
	s_waitcnt lgkmcnt(1)
	v_mfma_f32_16x16x32_bf16 v[74:77], v[118:121], v[74:77], v[114:117]
	v_xor_b32_e32 v80, 0x80000000, v72
	s_addc_u32 s29, s18, s53
	s_add_u32 s2, s19, s52
	v_and_or_b32 v114, v84, s80, v83
	v_cvt_pk_bf16_f32 v81, v81, v81
	v_cvt_pk_bf16_f32 v80, v80, v80
	v_lshrrev_b32_e32 v80, 16, v80
	v_and_or_b32 v115, v81, s80, v80
	v_mov_b32_e32 v80, v35
	v_mov_b32_e32 v81, v35
	v_mov_b32_e32 v116, v35
	v_mov_b32_e32 v117, v35
	v_lshlrev_b32_e32 v32, 2, v82
	s_addc_u32 s3, s66, s53
	s_waitcnt lgkmcnt(0)
	v_mfma_f32_16x16x32_bf16 v[74:77], v[78:81], v[114:117], v[74:77]
	ds_read_b64 v[78:79], v33 offset:55296
	s_add_u32 s52, s21, s52
	s_addc_u32 s53, s70, s53
	s_and_b64 vcc, exec, s[48:49]
	s_nop 3
	v_cvt_pk_bf16_f32 v74, v74, v75
	v_cvt_pk_bf16_f32 v75, v76, v77
	v_cvt_pk_bf16_f32 v62, v62, v63
	v_cvt_pk_bf16_f32 v63, v64, v65
	v_cvt_pk_bf16_f32 v64, v66, v67
	v_cvt_pk_bf16_f32 v65, v68, v69
	v_mov_b32_e32 v76, v35
	v_mov_b32_e32 v77, v35
	s_waitcnt lgkmcnt(0)
	s_nop 0
	v_mfma_f32_16x16x32_bf16 v[74:77], v[78:81], v[74:77], 0
	v_cvt_pk_bf16_f32 v66, v70, v71
	v_cvt_pk_bf16_f32 v67, v72, v73
	s_nop 5
	v_cvt_pk_bf16_f32 v68, v74, v75
	v_cvt_pk_bf16_f32 v69, v76, v77
	v_ashrrev_i32_e32 v33, 31, v32
	v_lshlrev_b32_e32 v70, 7, v45
	v_mov_b32_e32 v71, v35
	v_lshlrev_b64 v[74:75], 1, v[32:33]
	v_mul_u32_u24_e32 v33, 0x48, v106
	v_lshl_add_u64 v[72:73], s[28:29], 0, v[70:71]
	v_lshl_add_u64 v[70:71], s[52:53], 0, v[70:71]
	v_lshl_add_u32 v33, v33, 1, v86
	v_lshl_add_u64 v[80:81], v[72:73], 0, v[74:75]
	v_lshl_add_u64 v[78:79], v[70:71], 0, v[74:75]
	v_add_u32_e32 v74, 0x9000, v33
	ds_read2_b64 v[70:73], v74 offset1:4
	ds_read2_b64 v[74:77], v74 offset0:8 offset1:12
	s_waitcnt lgkmcnt(1)
	v_mfma_f32_16x16x32_bf16 v[70:73], v[70:73], v[62:65], 0
	v_add_u32_e32 v33, 0xb000, v33
	ds_read2_b64 v[106:109], v33 offset0:136 offset1:140
	s_mov_b64 s[28:29], -1
	s_waitcnt lgkmcnt(1)
	v_mfma_f32_16x16x32_bf16 v[70:73], v[74:77], v[66:69], v[70:73]
	ds_read2_b64 v[74:77], v33 offset0:128 offset1:132
	s_waitcnt lgkmcnt(0)
	v_mfma_f32_16x16x32_bf16 v[74:77], v[74:77], v[62:65], 0
	v_mfma_f32_16x16x32_bf16 v[74:77], v[106:109], v[66:69], v[74:77]
	v_mul_u32_u24_e32 v218, 0x48, v89
	v_lshl_add_u32 v218, v218, 1, v86
	v_add_u32_e32 v219, 0x9000, v218
	v_add_u32_e32 v218, 0xb000, v218
	ds_read2_b64 v[202:205], v219 offset1:4
	ds_read2_b64 v[206:209], v219 offset0:8 offset1:12
	ds_read2_b64 v[210:213], v218 offset0:136 offset1:140
	ds_read2_b64 v[214:217], v218 offset0:128 offset1:132
	s_cbranch_vccnz .LBB0_1783
	s_nop 2
	v_cvt_pk_bf16_f32 v84, v70, v71
	v_cvt_pk_bf16_f32 v85, v72, v73
	global_store_dwordx2 v[80:81], v[84:85], off
	s_nop 0
	v_cvt_pk_bf16_f32 v84, v74, v75
	v_cvt_pk_bf16_f32 v85, v76, v77
	s_mov_b64 s[28:29], 0
	global_store_dwordx2 v[78:79], v[84:85], off

; #define LAS __attribute__((address_space(3)))
; __device__ __forceinline__ unsigned f2bf(float f) { unsigned u = __float_as_uint(f); return (u + 0x7fffu + ((u >> 16) & 1u)) >> 16; }
; __device__ __forceinline__ u32x2 cvt4(f32x4 v) { return (u32x2){pk2(v[0], v[1]), pk2(v[2], v[3])}; }
; __device__ __forceinline__ void gdn_s23(CArgs& a, int u, const GdnIn2& in, LAS unsigned char* ub, LAS unsigned char* dwb, int w, int lane, float cl) {
;     ...
;     bf16* ftp = FTo + (c0 + fr) * 64 + 4 * kg; bf16* btp = BTo + (c0 + fr) * 64 + 4 * kg; bf16* ep = Eo + (4 * kg) * 64 + c0 + fr; bf16* mp = Mo + (4 * kg) * 64 + c0 + fr;
; #pragma unroll
;     for (int t4 = 0; t4 < 4; ++t4) {
;         const LAS bf16* ar = ATT + (16 * t4 + fr) * 72 + 4 * kg; const LAS bf16* kr = KTT + (16 * t4 + fr) * 72 + 4 * kg;
;         f32x4 pa = (f32x4){0.f, 0.f, 0.f, 0.f}, pk = (f32x4){0.f, 0.f, 0.f, 0.f};
;         pa = __builtin_amdgcn_mfma_f32_16x16x32_bf16(frag2(*(const LAS u32x2*)ar, *(const LAS u32x2*)(ar + 16)), Xb01, pa, 0, 0, 0);
;         pa = __builtin_amdgcn_mfma_f32_16x16x32_bf16(frag2(*(const LAS u32x2*)(ar + 32), *(const LAS u32x2*)(ar + 48)), Xb23, pa, 0, 0, 0);
;         pk = __builtin_amdgcn_mfma_f32_16x16x32_bf16(frag2(*(const LAS u32x2*)kr, *(const LAS u32x2*)(kr + 16)), Xb01, pk, 0, 0, 0);
;         pk = __builtin_amdgcn_mfma_f32_16x16x32_bf16(frag2(*(const LAS u32x2*)(kr + 32), *(const LAS u32x2*)(kr + 48)), Xb23, pk, 0, 0, 0);
;         if (!isW) {
;             *(u32x2*)(ftp + 16 * t4) = cvt4(pa);
;             *(u32x2*)(btp + 16 * t4) = cvt4(pk);
;         } else {
;             const f32x4 ec = *(const LAS f32x4*)(GT + 128 + 16 * t4 + 4 * kg);
; #pragma unroll
;             for (int e = 0; e < 4; ++e) { const int row = 16 * t4 + 4 * kg + e, col = c0 + fr;
;                 ep[(16 * t4 + e) * 64] = (bf16)f2bf(ec[e] * __uint_as_float(in.Qv[t4][e] << 16) - pa[e]);
;                 mp[(16 * t4 + e) * 64] = (bf16)f2bf((row == col ? ecl : 0.f) - pk[e]); }
;         }
;     }
.LBB0_1785:
	s_mov_b64 s[2:3], -1
	s_and_b64 vcc, exec, s[48:49]
	s_waitcnt lgkmcnt(0)
	v_mfma_f32_16x16x32_bf16 v[54:57], v[202:205], v[62:65], 0
	v_mfma_f32_16x16x32_bf16 v[54:57], v[206:209], v[66:69], v[54:57]
	v_mfma_f32_16x16x32_bf16 v[70:73], v[214:217], v[62:65], 0
	v_mfma_f32_16x16x32_bf16 v[70:73], v[210:213], v[66:69], v[70:73]
	v_mul_u32_u24_e32 v218, 0x48, v88
	v_lshl_add_u32 v218, v218, 1, v86
	v_add_u32_e32 v219, 0x9000, v218
	v_add_u32_e32 v218, 0xb000, v218
	ds_read2_b64 v[226:229], v219 offset1:4
	ds_read2_b64 v[230:233], v219 offset0:8 offset1:12
	ds_read2_b64 v[234:237], v218 offset0:136 offset1:140
	ds_read2_b64 v[238:241], v218 offset0:128 offset1:132
	s_cbranch_vccnz .LBB0_1787
	s_nop 2
	v_cvt_pk_bf16_f32 v74, v54, v55
	v_cvt_pk_bf16_f32 v75, v56, v57
	global_store_dwordx2 v[80:81], v[74:75], off offset:32
	s_nop 0
	v_cvt_pk_bf16_f32 v74, v70, v71
	v_cvt_pk_bf16_f32 v34, v72, v72
	v_lshrrev_b32_e32 v34, 16, v34
	v_cvt_pk_bf16_f32 v75, v73, v73
	v_and_or_b32 v75, v75, s80, v34
	s_mov_b64 s[2:3], 0
	global_store_dwordx2 v[78:79], v[74:75], off offset:32

; #define LAS __attribute__((address_space(3)))
; __device__ __forceinline__ unsigned f2bf(float f) { unsigned u = __float_as_uint(f); return (u + 0x7fffu + ((u >> 16) & 1u)) >> 16; }
; __device__ __forceinline__ u32x2 cvt4(f32x4 v) { return (u32x2){pk2(v[0], v[1]), pk2(v[2], v[3])}; }
; __device__ __forceinline__ void gdn_s23(CArgs& a, int u, const GdnIn2& in, LAS unsigned char* ub, LAS unsigned char* dwb, int w, int lane, float cl) {
;     ...
;     bf16* ftp = FTo + (c0 + fr) * 64 + 4 * kg; bf16* btp = BTo + (c0 + fr) * 64 + 4 * kg; bf16* ep = Eo + (4 * kg) * 64 + c0 + fr; bf16* mp = Mo + (4 * kg) * 64 + c0 + fr;
; #pragma unroll
;     for (int t4 = 0; t4 < 4; ++t4) {
;         const LAS bf16* ar = ATT + (16 * t4 + fr) * 72 + 4 * kg; const LAS bf16* kr = KTT + (16 * t4 + fr) * 72 + 4 * kg;
;         f32x4 pa = (f32x4){0.f, 0.f, 0.f, 0.f}, pk = (f32x4){0.f, 0.f, 0.f, 0.f};
;         pa = __builtin_amdgcn_mfma_f32_16x16x32_bf16(frag2(*(const LAS u32x2*)ar, *(const LAS u32x2*)(ar + 16)), Xb01, pa, 0, 0, 0);
;         pa = __builtin_amdgcn_mfma_f32_16x16x32_bf16(frag2(*(const LAS u32x2*)(ar + 32), *(const LAS u32x2*)(ar + 48)), Xb23, pa, 0, 0, 0);
;         pk = __builtin_amdgcn_mfma_f32_16x16x32_bf16(frag2(*(const LAS u32x2*)kr, *(const LAS u32x2*)(kr + 16)), Xb01, pk, 0, 0, 0);
;         pk = __builtin_amdgcn_mfma_f32_16x16x32_bf16(frag2(*(const LAS u32x2*)(kr + 32), *(const LAS u32x2*)(kr + 48)), Xb23, pk, 0, 0, 0);
;         if (!isW) {
;             *(u32x2*)(ftp + 16 * t4) = cvt4(pa);
;             *(u32x2*)(btp + 16 * t4) = cvt4(pk);
;         } else {
;             const f32x4 ec = *(const LAS f32x4*)(GT + 128 + 16 * t4 + 4 * kg);
; #pragma unroll
;             for (int e = 0; e < 4; ++e) { const int row = 16 * t4 + 4 * kg + e, col = c0 + fr;
;                 ep[(16 * t4 + e) * 64] = (bf16)f2bf(ec[e] * __uint_as_float(in.Qv[t4][e] << 16) - pa[e]);
;                 mp[(16 * t4 + e) * 64] = (bf16)f2bf((row == col ? ecl : 0.f) - pk[e]); }
;         }
;     }
.LBB0_1789:
	s_mov_b64 s[2:3], -1
	s_and_b64 vcc, exec, s[48:49]
	s_waitcnt lgkmcnt(0)
	v_mfma_f32_16x16x32_bf16 v[50:53], v[226:229], v[62:65], 0
	v_mfma_f32_16x16x32_bf16 v[50:53], v[230:233], v[66:69], v[50:53]
	v_mfma_f32_16x16x32_bf16 v[54:57], v[238:241], v[62:65], 0
	v_mfma_f32_16x16x32_bf16 v[54:57], v[234:237], v[66:69], v[54:57]
	v_mul_u32_u24_e32 v218, 0x48, v87
	v_lshl_add_u32 v218, v218, 1, v86
	v_add_u32_e32 v219, 0x9000, v218
	v_add_u32_e32 v218, 0xb000, v218
	ds_read2_b64 v[202:205], v219 offset1:4
	ds_read2_b64 v[206:209], v219 offset0:8 offset1:12
	ds_read2_b64 v[210:213], v218 offset0:128 offset1:132
	ds_read2_b64 v[214:217], v218 offset0:136 offset1:140
	s_cbranch_vccnz .LBB0_1791
	s_nop 2
	v_cvt_pk_bf16_f32 v70, v50, v51
	v_cvt_pk_bf16_f32 v71, v52, v53
	global_store_dwordx2 v[80:81], v[70:71], off offset:64
	s_nop 0
	v_cvt_pk_bf16_f32 v70, v54, v55
	v_cvt_pk_bf16_f32 v34, v56, v56
	v_lshrrev_b32_e32 v34, 16, v34
	v_cvt_pk_bf16_f32 v71, v57, v57
	v_and_or_b32 v71, v71, s80, v34
	s_mov_b64 s[2:3], 0
	global_store_dwordx2 v[78:79], v[70:71], off offset:64

; #define LAS __attribute__((address_space(3)))
; __device__ __forceinline__ unsigned f2bf(float f) { unsigned u = __float_as_uint(f); return (u + 0x7fffu + ((u >> 16) & 1u)) >> 16; }
; __device__ __forceinline__ u32x2 cvt4(f32x4 v) { return (u32x2){pk2(v[0], v[1]), pk2(v[2], v[3])}; }
; __device__ __forceinline__ void gdn_s23(CArgs& a, int u, const GdnIn2& in, LAS unsigned char* ub, LAS unsigned char* dwb, int w, int lane, float cl) {
;     ...
;     bf16* ftp = FTo + (c0 + fr) * 64 + 4 * kg; bf16* btp = BTo + (c0 + fr) * 64 + 4 * kg; bf16* ep = Eo + (4 * kg) * 64 + c0 + fr; bf16* mp = Mo + (4 * kg) * 64 + c0 + fr;
; #pragma unroll
;     for (int t4 = 0; t4 < 4; ++t4) {
;         const LAS bf16* ar = ATT + (16 * t4 + fr) * 72 + 4 * kg; const LAS bf16* kr = KTT + (16 * t4 + fr) * 72 + 4 * kg;
;         f32x4 pa = (f32x4){0.f, 0.f, 0.f, 0.f}, pk = (f32x4){0.f, 0.f, 0.f, 0.f};
;         pa = __builtin_amdgcn_mfma_f32_16x16x32_bf16(frag2(*(const LAS u32x2*)ar, *(const LAS u32x2*)(ar + 16)), Xb01, pa, 0, 0, 0);
;         pa = __builtin_amdgcn_mfma_f32_16x16x32_bf16(frag2(*(const LAS u32x2*)(ar + 32), *(const LAS u32x2*)(ar + 48)), Xb23, pa, 0, 0, 0);
;         pk = __builtin_amdgcn_mfma_f32_16x16x32_bf16(frag2(*(const LAS u32x2*)kr, *(const LAS u32x2*)(kr + 16)), Xb01, pk, 0, 0, 0);
;         pk = __builtin_amdgcn_mfma_f32_16x16x32_bf16(frag2(*(const LAS u32x2*)(kr + 32), *(const LAS u32x2*)(kr + 48)), Xb23, pk, 0, 0, 0);
;         if (!isW) {
;             *(u32x2*)(ftp + 16 * t4) = cvt4(pa);
;             *(u32x2*)(btp + 16 * t4) = cvt4(pk);
;         } else {
;             const f32x4 ec = *(const LAS f32x4*)(GT + 128 + 16 * t4 + 4 * kg);
; #pragma unroll
;             for (int e = 0; e < 4; ++e) { const int row = 16 * t4 + 4 * kg + e, col = c0 + fr;
;                 ep[(16 * t4 + e) * 64] = (bf16)f2bf(ec[e] * __uint_as_float(in.Qv[t4][e] << 16) - pa[e]);
;                 mp[(16 * t4 + e) * 64] = (bf16)f2bf((row == col ? ecl : 0.f) - pk[e]); }
;         }
;     }
.LBB0_1793:
	s_and_b64 vcc, exec, s[48:49]
	s_mov_b64 s[2:3], -1
	s_waitcnt lgkmcnt(0)
	v_mfma_f32_16x16x32_bf16 v[50:53], v[202:205], v[62:65], 0
	v_mfma_f32_16x16x32_bf16 v[50:53], v[206:209], v[66:69], v[50:53]
	v_mfma_f32_16x16x32_bf16 v[54:57], v[210:213], v[62:65], 0
	v_mfma_f32_16x16x32_bf16 v[54:57], v[214:217], v[66:69], v[54:57]
	s_cbranch_vccnz .LBB0_1795
	s_nop 1
	s_nop 2
	v_cvt_pk_bf16_f32 v58, v50, v51
	v_cvt_pk_bf16_f32 v59, v52, v53
	global_store_dwordx2 v[80:81], v[58:59], off offset:96
	s_nop 1
	v_cvt_pk_bf16_f32 v58, v54, v55
	v_cvt_pk_bf16_f32 v34, v56, v56
	v_lshrrev_b32_e32 v34, 16, v34
	v_cvt_pk_bf16_f32 v59, v57, v57
	v_and_or_b32 v59, v59, s80, v34
	global_store_dwordx2 v[78:79], v[58:59], off offset:96
	s_cbranch_execnz .LBB0_1682
	s_branch .LBB0_1796
